# speedup vs baseline: 1.0352x; 1.0352x over previous
_Z9fast_mainILb0EEvPKiS1_S1_PKfPKcS3_PfS6_PiPyS6_:
	s_load_dwordx4 s[4:7], s[0:1], 0x20
	s_load_dwordx4 s[8:11], s[0:1], 0x8
	v_and_b32_e32 v1, 63, v0
	v_lshrrev_b32_e32 v8, 6, v0
	v_lshlrev_b32_e32 v150, 4, v1
	v_add_u32_e32 v212, 0x10000, v150
	v_add_u32_e32 v213, 0x18c00, v150
	v_mov_b32_e32 v151, 0
	s_waitcnt lgkmcnt(0)
	v_lshl_add_u64 v[4:5], s[4:5], 0, v[150:151]
	v_lshlrev_b32_e32 v2, 10, v8
	v_mov_b32_e32 v3, v151
	v_lshl_add_u64 v[6:7], v[4:5], 0, v[2:3]
	v_readfirstlane_b32 s3, v2
	v_or_b32_e32 v3, 0x2000, v2
	s_mov_b32 m0, s3
	s_mov_b64 s[4:5], 0x2000
	v_readfirstlane_b32 s3, v3
	global_load_lds_dwordx4 v[6:7], off
	v_lshl_add_u64 v[10:11], v[6:7], 0, s[4:5]
	s_mov_b32 m0, s3
	v_or_b32_e32 v3, 0x6000, v2
	global_load_lds_dwordx4 v[10:11], off
	v_or_b32_e32 v10, 0x4000, v2
	v_mov_b32_e32 v11, v151
	v_readfirstlane_b32 s3, v10
	v_lshl_add_u64 v[12:13], v[4:5], 0, v[10:11]
	s_mov_b32 m0, s3
	s_mov_b64 s[4:5], 0x6000
	v_readfirstlane_b32 s3, v3
	global_load_lds_dwordx4 v[12:13], off
	v_lshl_add_u64 v[10:11], v[6:7], 0, s[4:5]
	s_mov_b32 m0, s3
	v_or_b32_e32 v3, 0xa000, v2
	global_load_lds_dwordx4 v[10:11], off
	v_or_b32_e32 v10, 0x8000, v2
	v_mov_b32_e32 v11, v151
	v_readfirstlane_b32 s3, v10
	v_lshl_add_u64 v[12:13], v[4:5], 0, v[10:11]
	s_mov_b32 m0, s3
	s_mov_b64 s[4:5], 0xa000
	v_readfirstlane_b32 s3, v3
	global_load_lds_dwordx4 v[12:13], off
	v_lshl_add_u64 v[10:11], v[6:7], 0, s[4:5]
	s_mov_b32 m0, s3
	v_or_b32_e32 v3, 0xe000, v2
	global_load_lds_dwordx4 v[10:11], off
	v_or_b32_e32 v10, 0xc000, v2
	v_mov_b32_e32 v11, v151
	v_readfirstlane_b32 s3, v10
	v_lshl_add_u64 v[12:13], v[4:5], 0, v[10:11]
	s_mov_b32 m0, s3
	s_mov_b64 s[4:5], 0xe000
	v_readfirstlane_b32 s3, v3
	global_load_lds_dwordx4 v[12:13], off
	v_lshl_add_u64 v[10:11], v[6:7], 0, s[4:5]
	s_mov_b32 m0, s3
	v_or_b32_e32 v3, 0x12000, v2
	global_load_lds_dwordx4 v[10:11], off
	v_or_b32_e32 v10, 0x10000, v2
	v_mov_b32_e32 v11, v151
	v_readfirstlane_b32 s3, v10
	v_lshl_add_u64 v[12:13], v[4:5], 0, v[10:11]
	s_mov_b32 m0, s3
	s_mov_b64 s[4:5], 0x12000
	v_readfirstlane_b32 s3, v3
	global_load_lds_dwordx4 v[12:13], off
	v_lshl_add_u64 v[10:11], v[6:7], 0, s[4:5]
	s_mov_b32 m0, s3
	s_nop 0
	global_load_lds_dwordx4 v[10:11], off
	v_or_b32_e32 v10, 0x14000, v2
	v_mov_b32_e32 v11, v151
	v_readfirstlane_b32 s3, v10
	v_lshl_add_u64 v[12:13], v[4:5], 0, v[10:11]
	s_mov_b32 m0, s3
	s_movk_i32 s3, 0x2c0
	global_load_lds_dwordx4 v[12:13], off
	v_cmp_gt_u32_e32 vcc, s3, v0
	s_and_saveexec_b64 s[4:5], vcc
	s_cbranch_execz .LBB1_2
	v_or_b32_e32 v3, 0x16000, v2
	s_mov_b64 s[12:13], 0x16000
	v_readfirstlane_b32 s3, v3
	v_lshl_add_u64 v[6:7], v[6:7], 0, s[12:13]
	s_mov_b32 m0, s3
	s_nop 0
	global_load_lds_dwordx4 v[6:7], off

.LBB1_6:
	s_or_saveexec_b64 s[4:5], s[4:5]
	s_load_dwordx4 s[8:11], s[0:1], 0x48
	s_xor_b64 exec, exec, s[4:5]
	s_cbranch_execz .LBB1_8
	v_lshlrev_b32_e32 v18, 7, v64
	v_or_b32_e32 v30, v18, v174
	ds_read_b128 v[2:5], v30 offset:35072
	ds_read_b128 v[6:9], v30 offset:35104
	ds_read_b128 v[10:13], v30 offset:35136
	ds_read_b128 v[14:17], v30 offset:35168
	v_mul_u32_u24_e32 v19, 0xf80, v64
	v_add3_u32 v62, v18, v19, v150
	s_movk_i32 s0, 0x80
	ds_read_b128 v[18:21], v62 offset:8192
	ds_read_b128 v[50:53], v150
	ds_read_b128 v[54:57], v150 offset:4096
	ds_read_b128 v[58:61], v62 offset:16384
	ds_read_b128 v[66:69], v150 offset:1024
	ds_read_b128 v[70:73], v150 offset:5120
	v_cmp_gt_u32_e32 vcc, s0, v0
	ds_read_b128 v[74:77], v62 offset:9216
	s_mov_b32 s0, 0x3e8293ee
	s_waitcnt lgkmcnt(0)
	v_cndmask_b32_e32 v25, v57, v53, vcc
	v_cndmask_b32_e32 v24, v56, v52, vcc
	v_cndmask_b32_e32 v23, v55, v51, vcc
	v_cndmask_b32_e32 v22, v54, v50, vcc
	s_nop 1
	v_mfma_f32_32x32x16_bf16 v[2:17], v[18:21], v[22:25], v[2:17]
	ds_read_b128 v[18:21], v30 offset:35328
	ds_read_b128 v[22:25], v30 offset:35360
	ds_read_b128 v[26:29], v30 offset:35392
	ds_read_b128 v[30:33], v30 offset:35424
	ds_read_b128 v[78:81], v62 offset:17408
	s_waitcnt lgkmcnt(1)
	v_mfma_f32_32x32x16_bf16 v[34:49], v[58:61], v[50:53], v[18:33]
	v_cndmask_b32_e32 v53, v73, v69, vcc
	v_cndmask_b32_e32 v52, v72, v68, vcc
	v_cndmask_b32_e32 v51, v71, v67, vcc
	v_cndmask_b32_e32 v50, v70, v66, vcc
	v_mfma_f32_32x32x16_bf16 v[18:33], v[58:61], v[54:57], v[18:33]
	s_nop 0
	v_mfma_f32_32x32x16_bf16 v[2:17], v[74:77], v[50:53], v[2:17]
	ds_read_b128 v[50:53], v150 offset:2048
	ds_read_b128 v[54:57], v150 offset:6144
	ds_read_b128 v[58:61], v62 offset:10240
	s_waitcnt lgkmcnt(1)
	v_cndmask_b32_e32 v77, v57, v53, vcc
	v_cndmask_b32_e32 v76, v56, v52, vcc
	v_cndmask_b32_e32 v75, v55, v51, vcc
	v_mfma_f32_32x32x16_bf16 v[34:49], v[78:81], v[66:69], v[34:49]
	v_cndmask_b32_e32 v74, v54, v50, vcc
	v_mfma_f32_32x32x16_bf16 v[18:33], v[78:81], v[70:73], v[18:33]
	ds_read_b128 v[66:69], v150 offset:3072
	ds_read_b128 v[70:73], v150 offset:7168
	ds_read_b128 v[78:81], v62 offset:11264
	s_waitcnt lgkmcnt(3)
	v_mfma_f32_32x32x16_bf16 v[2:17], v[58:61], v[74:77], v[2:17]
	ds_read_b128 v[58:61], v62 offset:18432
	ds_read_b128 v[74:77], v62 offset:19456
	s_waitcnt lgkmcnt(1)
	v_mfma_f32_32x32x16_bf16 v[34:49], v[58:61], v[50:53], v[34:49]
	v_cndmask_b32_e32 v53, v73, v69, vcc
	v_cndmask_b32_e32 v52, v72, v68, vcc
	v_cndmask_b32_e32 v51, v71, v67, vcc
	v_cndmask_b32_e32 v50, v70, v66, vcc
	v_mfma_f32_32x32x16_bf16 v[18:33], v[58:61], v[54:57], v[18:33]
	s_nop 0
	v_mfma_f32_32x32x16_bf16 v[2:17], v[78:81], v[50:53], v[2:17]
	s_waitcnt lgkmcnt(0)
	v_mfma_f32_32x32x16_bf16 v[34:49], v[74:77], v[66:69], v[34:49]
	s_nop 9
	v_cvt_pk_bf16_f32 v9, v8, v9
	v_cvt_pk_bf16_f32 v8, v6, v7
	v_cvt_pk_bf16_f32 v7, v4, v5
	v_cvt_pk_bf16_f32 v6, v2, v3
	v_mfma_f32_32x32x16_bf16 v[18:33], v[74:77], v[70:73], v[18:33]
	v_cvt_pk_bf16_f32 v5, v40, v41
	v_cvt_pk_bf16_f32 v4, v38, v39
	v_cvt_pk_bf16_f32 v3, v36, v37
	v_cvt_pk_bf16_f32 v2, v34, v35
	v_cvt_pk_bf16_f32 v36, v14, v15
	v_cvt_pk_bf16_f32 v15, v48, v49
	v_cvt_pk_bf16_f32 v35, v12, v13
	v_mfma_f32_32x32x16_bf16 v[48:63], v[2:5], v[6:9], 0
	v_cvt_pk_bf16_f32 v14, v46, v47
	v_cvt_pk_bf16_f32 v13, v44, v45
	v_cvt_pk_bf16_f32 v12, v42, v43
	s_nop 0
	v_cvt_pk_bf16_f32 v5, v24, v25
	v_cvt_pk_bf16_f32 v4, v22, v23
	v_cvt_pk_bf16_f32 v3, v20, v21
	v_cvt_pk_bf16_f32 v2, v18, v19
	v_cvt_pk_bf16_f32 v37, v16, v17
	v_cvt_pk_bf16_f32 v34, v10, v11
	v_cvt_pk_bf16_f32 v21, v32, v33
	v_cvt_pk_bf16_f32 v20, v30, v31
	v_mfma_f32_32x32x16_bf16 v[48:63], v[12:15], v[34:37], v[48:63]
	v_cvt_pk_bf16_f32 v19, v28, v29
	v_cvt_pk_bf16_f32 v18, v26, v27
	v_mfma_f32_32x32x16_bf16 v[2:17], v[2:5], v[6:9], 0
	s_nop 8
	v_mul_f32_e64 v22, v62, s0
	v_mul_f32_e64 v23, v63, s0
	v_mul_f32_e64 v24, v60, s0
	v_mul_f32_e64 v25, v61, s0
	v_mul_f32_e64 v26, v58, s0
	v_mul_f32_e64 v27, v59, s0
	v_pk_mul_f32 v[28:29], v[56:57], s[0:1] op_sel_hi:[1,0]
	v_pk_mul_f32 v[30:31], v[54:55], s[0:1] op_sel_hi:[1,0]
	v_pk_mul_f32 v[32:33], v[52:53], s[0:1] op_sel_hi:[1,0]
	v_pk_mul_f32 v[38:39], v[50:51], s[0:1] op_sel_hi:[1,0]
	v_mfma_f32_32x32x16_bf16 v[2:17], v[18:21], v[34:37], v[2:17]
	v_mul_f32_e64 v40, v48, s0
	v_mul_f32_e64 v41, v49, s0
	s_nop 9
	v_pk_mul_f32 v[16:17], v[16:17], s[0:1] op_sel_hi:[1,0]
	v_pk_mul_f32 v[14:15], v[14:15], s[0:1] op_sel_hi:[1,0]
	v_pk_mul_f32 v[12:13], v[12:13], s[0:1] op_sel_hi:[1,0]
	v_pk_mul_f32 v[10:11], v[10:11], s[0:1] op_sel_hi:[1,0]
	v_pk_mul_f32 v[18:19], v[8:9], s[0:1] op_sel_hi:[1,0]
	v_pk_mul_f32 v[20:21], v[6:7], s[0:1] op_sel_hi:[1,0]
	v_pk_mul_f32 v[34:35], v[4:5], s[0:1] op_sel_hi:[1,0]
	v_pk_mul_f32 v[36:37], v[2:3], s[0:1] op_sel_hi:[1,0]
	s_mov_b32 s0, 0xff800000
	v_max3_f32 v2, v40, s0, v41
	v_max3_f32 v2, v2, v38, v39
	v_max3_f32 v2, v2, v32, v33
	v_max3_f32 v2, v2, v30, v31
	v_max3_f32 v2, v2, v28, v29
	v_max3_f32 v2, v2, v26, v27
	v_max3_f32 v2, v2, v24, v25
	v_max3_f32 v2, v2, v22, v23
	v_max3_f32 v2, v2, v36, v37
	v_max3_f32 v2, v2, v34, v35
	v_max3_f32 v2, v2, v20, v21
	v_max3_f32 v2, v2, v18, v19
	v_max3_f32 v2, v2, v10, v11
	v_max3_f32 v2, v2, v12, v13
	v_max3_f32 v2, v2, v14, v15
	v_max3_f32 v2, v2, v16, v17
	v_mov_b32_e32 v3, v2
	s_nop 1
	v_permlane32_swap_b32_e32 v2, v3
	v_max_f32_e32 v42, v2, v3
	v_lshlrev_b32_e32 v3, 6, v0
	v_lshlrev_b32_e32 v2, 14, v64
	v_and_b32_e32 v3, 0x2000, v3
	v_or3_b32 v43, v2, v3, v150
	v_sub_f32_e32 v2, v40, v42
	v_sub_f32_e32 v3, v41, v42
	v_sub_f32_e32 v4, v38, v42
	v_sub_f32_e32 v5, v39, v42
	v_exp_f32_e32 v2, v2
	v_exp_f32_e32 v3, v3
	v_exp_f32_e32 v4, v4
	v_exp_f32_e32 v5, v5
	v_sub_f32_e32 v6, v32, v42
	v_sub_f32_e32 v7, v33, v42
	v_sub_f32_e32 v8, v30, v42
	v_sub_f32_e32 v9, v31, v42
	v_exp_f32_e32 v6, v6
	v_exp_f32_e32 v7, v7
	v_exp_f32_e32 v8, v8
	v_exp_f32_e32 v9, v9
	v_or_b32_e32 v30, 0x18c00, v43
	ds_write_b128 v30, v[2:5]
	v_or_b32_e32 v2, 0x19000, v43
	ds_write_b128 v2, v[6:9]
	v_sub_f32_e32 v2, v28, v42
	v_sub_f32_e32 v3, v29, v42
	v_sub_f32_e32 v4, v26, v42
	v_sub_f32_e32 v5, v27, v42
	v_exp_f32_e32 v2, v2
	v_exp_f32_e32 v3, v3
	v_exp_f32_e32 v4, v4
	v_exp_f32_e32 v5, v5
	v_sub_f32_e32 v6, v24, v42
	v_sub_f32_e32 v7, v25, v42
	v_sub_f32_e32 v8, v22, v42
	v_sub_f32_e32 v9, v23, v42
	v_exp_f32_e32 v6, v6
	v_exp_f32_e32 v7, v7
	v_exp_f32_e32 v8, v8
	v_exp_f32_e32 v9, v9
	v_or_b32_e32 v22, 0x19400, v43
	ds_write_b128 v22, v[2:5]
	v_or_b32_e32 v2, 0x19800, v43
	ds_write_b128 v2, v[6:9]
	v_sub_f32_e32 v2, v36, v42
	v_sub_f32_e32 v3, v37, v42
	v_sub_f32_e32 v4, v34, v42
	v_sub_f32_e32 v5, v35, v42
	v_exp_f32_e32 v2, v2
	v_exp_f32_e32 v3, v3
	v_exp_f32_e32 v4, v4
	v_exp_f32_e32 v5, v5
	v_sub_f32_e32 v6, v20, v42
	v_sub_f32_e32 v7, v21, v42
	v_sub_f32_e32 v8, v18, v42
	v_sub_f32_e32 v9, v19, v42
	v_exp_f32_e32 v6, v6
	v_exp_f32_e32 v7, v7
	v_exp_f32_e32 v8, v8
	v_exp_f32_e32 v9, v9
	v_or_b32_e32 v18, 0x19c00, v43
	ds_write_b128 v18, v[2:5]
	v_add_u32_e32 v2, 0x1a000, v43
	ds_write_b128 v2, v[6:9]
	v_sub_f32_e32 v2, v10, v42
	v_sub_f32_e32 v3, v11, v42
	v_sub_f32_e32 v4, v12, v42
	v_sub_f32_e32 v5, v13, v42
	v_exp_f32_e32 v2, v2
	v_exp_f32_e32 v3, v3
	v_exp_f32_e32 v4, v4
	v_exp_f32_e32 v5, v5
	v_sub_f32_e32 v6, v14, v42
	v_sub_f32_e32 v7, v15, v42
	v_sub_f32_e32 v8, v16, v42
	v_sub_f32_e32 v9, v17, v42
	v_exp_f32_e32 v6, v6
	v_exp_f32_e32 v7, v7
	v_exp_f32_e32 v8, v8
	v_exp_f32_e32 v9, v9
	v_add_u32_e32 v10, 0x1a400, v43
	ds_write_b128 v10, v[2:5]
	v_add_u32_e32 v2, 0x1a800, v43
	ds_write_b128 v2, v[6:9]
	v_mov_b32_e32 v2, v174
.LBB1_8:
	s_or_b64 exec, exec, s[4:5]
	v_add_u32_e32 v10, v172, v2
	s_waitcnt lgkmcnt(0)
	s_barrier
	ds_read_b128 v[18:21], v10 offset:256
	ds_read_b128 v[22:25], v10 offset:288
	ds_read_b128 v[82:85], v10 offset:320
	ds_read_b128 v[86:89], v10 offset:352
	ds_read_b128 v[74:77], v10 offset:384
	ds_read_b128 v[78:81], v10 offset:416
	ds_read_b128 v[2:5], v213 offset:32768
	ds_read_b128 v[6:9], v213 offset:0
	ds_read_b128 v[66:69], v10 offset:448
	ds_read_b128 v[70:73], v10 offset:480
	ds_read_b128 v[10:13], v213 offset:1024
	s_waitcnt lgkmcnt(3)
	v_pk_mul_f32 v[26:27], v[8:9], v[20:21]
	v_pk_mul_f32 v[28:29], v[6:7], v[18:19]
	ds_read_b128 v[14:17], v213 offset:8192
	s_waitcnt lgkmcnt(1)
	v_pk_mul_f32 v[12:13], v[12:13], v[24:25]
	v_pk_mul_f32 v[10:11], v[10:11], v[22:23]
	v_pk_fma_f32 v[30:31], v[8:9], v[20:21], v[12:13]
	v_pk_fma_f32 v[32:33], v[6:7], v[18:19], v[10:11]
	v_cvt_pk_bf16_f32 v9, v12, v13
	v_cvt_pk_bf16_f32 v7, v26, v27
	v_cvt_pk_bf16_f32 v8, v10, v11
	v_cvt_pk_bf16_f32 v6, v28, v29
	ds_read_b128 v[10:13], v213 offset:33792
	s_nop 0
	v_mfma_f32_32x32x16_bf16 v[34:49], v[2:5], v[6:9], 0
	ds_read_b128 v[6:9], v213 offset:9216
	s_waitcnt lgkmcnt(2)
	v_mul_f32_e64 v26, v16, v20
	v_mul_f32_e64 v27, v17, v21
	v_pk_mul_f32 v[50:51], v[14:15], v[18:19]
	s_mov_b32 s4, 0x3727c5ac
	s_waitcnt lgkmcnt(0)
	v_pk_mul_f32 v[8:9], v[8:9], v[24:25]
	v_pk_mul_f32 v[28:29], v[6:7], v[22:23]
	v_pk_fma_f32 v[90:91], v[16:17], v[20:21], v[8:9]
	v_pk_fma_f32 v[92:93], v[14:15], v[18:19], v[28:29]
	ds_read_b128 v[14:17], v213 offset:2048
	v_cvt_pk_bf16_f32 v9, v8, v9
	v_cvt_pk_bf16_f32 v7, v26, v27
	v_cvt_pk_bf16_f32 v8, v28, v29
	ds_read_b128 v[26:29], v213 offset:3072
	v_cvt_pk_bf16_f32 v6, v50, v51
	s_waitcnt lgkmcnt(1)
	v_pk_mul_f32 v[94:95], v[14:15], v[82:83]
	s_mov_b32 s0, 0x3c800000
	v_mfma_f32_32x32x16_bf16 v[50:65], v[2:5], v[6:9], 0
	v_mul_f32_e64 v2, v16, v84
	v_mul_f32_e64 v3, v17, v85
	s_waitcnt lgkmcnt(0)
	v_mul_f32_e64 v4, v28, v88
	v_mul_f32_e64 v5, v29, v89
	v_pk_mul_f32 v[6:7], v[26:27], v[86:87]
	v_pk_fma_f32 v[8:9], v[16:17], v[84:85], v[4:5]
	v_cvt_pk_bf16_f32 v3, v2, v3
	v_pk_fma_f32 v[14:15], v[14:15], v[82:83], v[6:7]
	v_pk_add_f32 v[26:27], v[8:9], v[30:31]
	v_cvt_pk_bf16_f32 v5, v4, v5
	v_cvt_pk_bf16_f32 v4, v6, v7
	ds_read_b128 v[6:9], v213 offset:10240
	v_pk_add_f32 v[28:29], v[14:15], v[32:33]
	ds_read_b128 v[14:17], v213 offset:11264
	v_cvt_pk_bf16_f32 v2, v94, v95
	s_waitcnt lgkmcnt(1)
	v_pk_mul_f32 v[30:31], v[6:7], v[82:83]
	v_mov_b64_e32 v[152:153], s[4:5]
	v_mfma_f32_32x32x16_bf16 v[34:49], v[10:13], v[2:5], v[34:49]
	v_mul_f32_e64 v2, v8, v84
	v_mul_f32_e64 v3, v9, v85
	s_waitcnt lgkmcnt(0)
	v_mul_f32_e64 v4, v16, v88
	v_mul_f32_e64 v5, v17, v89
	v_pk_mul_f32 v[14:15], v[14:15], v[86:87]
	v_pk_fma_f32 v[8:9], v[8:9], v[84:85], v[4:5]
	v_pk_fma_f32 v[6:7], v[6:7], v[82:83], v[14:15]
	v_cvt_pk_bf16_f32 v5, v4, v5
	v_cvt_pk_bf16_f32 v3, v2, v3
	v_cvt_pk_bf16_f32 v4, v14, v15
	v_pk_add_f32 v[32:33], v[8:9], v[90:91]
	v_pk_add_f32 v[90:91], v[6:7], v[92:93]
	ds_read_b128 v[6:9], v213 offset:34816
	ds_read_b128 v[14:17], v213 offset:4096
	v_cvt_pk_bf16_f32 v2, v30, v31
	s_mov_b32 s13, 0
	s_mov_b64 s[6:7], 0
	v_mfma_f32_32x32x16_bf16 v[50:65], v[10:13], v[2:5], v[50:65]
	ds_read_b128 v[2:5], v213 offset:5120
	ds_read_b128 v[10:13], v213 offset:12288
	s_waitcnt lgkmcnt(2)
	v_pk_mul_f32 v[30:31], v[16:17], v[76:77]
	v_pk_mul_f32 v[92:93], v[14:15], v[74:75]
	s_waitcnt lgkmcnt(1)
	v_pk_mul_f32 v[4:5], v[4:5], v[80:81]
	v_pk_mul_f32 v[94:95], v[2:3], v[78:79]
	v_pk_fma_f32 v[2:3], v[16:17], v[76:77], v[4:5]
	v_cvt_pk_bf16_f32 v5, v4, v5
	v_pk_add_f32 v[96:97], v[2:3], v[26:27]
	v_cvt_pk_bf16_f32 v3, v30, v31
	v_cvt_pk_bf16_f32 v4, v94, v95
	v_cvt_pk_bf16_f32 v2, v92, v93
	v_pk_fma_f32 v[14:15], v[14:15], v[74:75], v[94:95]
	s_waitcnt lgkmcnt(0)
	v_pk_mul_f32 v[30:31], v[10:11], v[74:75]
	v_mfma_f32_32x32x16_bf16 v[34:49], v[6:9], v[2:5], v[34:49]
	ds_read_b128 v[2:5], v213 offset:13312
	v_add_f32_e64 v98, v14, v28
	v_add_f32_e64 v99, v15, v29
	ds_read_b128 v[14:17], v213 offset:35840
	v_pk_mul_f32 v[26:27], v[12:13], v[76:77]
	s_waitcnt lgkmcnt(1)
	v_pk_mul_f32 v[4:5], v[4:5], v[80:81]
	v_pk_mul_f32 v[28:29], v[2:3], v[78:79]
	v_pk_fma_f32 v[2:3], v[12:13], v[76:77], v[4:5]
	v_pk_fma_f32 v[10:11], v[10:11], v[74:75], v[28:29]
	v_pk_add_f32 v[32:33], v[2:3], v[32:33]
	v_pk_add_f32 v[92:93], v[10:11], v[90:91]
	ds_read_b128 v[10:13], v213 offset:6144
	v_cvt_pk_bf16_f32 v5, v4, v5
	v_cvt_pk_bf16_f32 v3, v26, v27
	v_cvt_pk_bf16_f32 v4, v28, v29
	ds_read_b128 v[26:29], v213 offset:7168
	v_cvt_pk_bf16_f32 v2, v30, v31
	s_waitcnt lgkmcnt(1)
	v_pk_mul_f32 v[30:31], v[10:11], v[66:67]
	v_mfma_f32_32x32x16_bf16 v[50:65], v[6:9], v[2:5], v[50:65]
	v_mul_f32_e64 v2, v12, v68
	v_mul_f32_e64 v3, v13, v69
	s_waitcnt lgkmcnt(0)
	v_mul_f32_e64 v4, v28, v72
	v_mul_f32_e64 v5, v29, v73
	v_pk_mul_f32 v[6:7], v[26:27], v[70:71]
	v_pk_fma_f32 v[8:9], v[12:13], v[68:69], v[4:5]
	v_cvt_pk_bf16_f32 v3, v2, v3
	v_pk_fma_f32 v[10:11], v[10:11], v[66:67], v[6:7]
	v_pk_add_f32 v[94:95], v[8:9], v[96:97]
	v_cvt_pk_bf16_f32 v5, v4, v5
	v_cvt_pk_bf16_f32 v4, v6, v7
	ds_read_b128 v[6:9], v213 offset:14336
	v_pk_add_f32 v[96:97], v[10:11], v[98:99]
	ds_read_b128 v[10:13], v213 offset:15360
	v_cvt_pk_bf16_f32 v2, v30, v31
	s_waitcnt lgkmcnt(1)
	v_pk_mul_f32 v[30:31], v[6:7], v[66:67]
	v_mfma_f32_32x32x16_bf16 v[34:49], v[14:17], v[2:5], v[34:49]
	s_waitcnt lgkmcnt(0)
	v_mul_f32_e64 v10, v10, v70
	v_mul_f32_e64 v11, v11, v71
	v_mul_f32_e64 v2, v8, v68
	v_mul_f32_e64 v3, v9, v69
	v_pk_mul_f32 v[4:5], v[12:13], v[72:73]
	v_pk_fma_f32 v[6:7], v[6:7], v[66:67], v[10:11]
	v_pk_fma_f32 v[8:9], v[8:9], v[68:69], v[4:5]
	v_pk_add_f32 v[92:93], v[6:7], v[92:93]
	v_cvt_pk_bf16_f32 v3, v2, v3
	v_pk_add_f32 v[90:91], v[8:9], v[32:33]
	v_cvt_pk_bf16_f32 v5, v4, v5
	v_cvt_pk_bf16_f32 v4, v10, v11
	ds_read_b128 v[26:29], v213 offset:36864
	ds_read_b128 v[6:9], v213 offset:16384
	v_cvt_pk_bf16_f32 v2, v30, v31
	ds_read_b128 v[98:101], v213 offset:25600
	ds_read_b128 v[102:105], v213 offset:37888
	v_mfma_f32_32x32x16_bf16 v[50:65], v[14:17], v[2:5], v[50:65]
	ds_read_b128 v[2:5], v213 offset:17408
	ds_read_b128 v[30:33], v213 offset:24576
	s_waitcnt lgkmcnt(4)
	v_pk_mul_f32 v[12:13], v[6:7], v[18:19]
	v_pk_mul_f32 v[10:11], v[8:9], v[20:21]
	s_waitcnt lgkmcnt(1)
	v_pk_mul_f32 v[14:15], v[2:3], v[22:23]
	v_pk_mul_f32 v[22:23], v[98:99], v[22:23]
	v_pk_fma_f32 v[112:113], v[6:7], v[18:19], v[14:15]
	s_waitcnt lgkmcnt(0)
	v_pk_mul_f32 v[114:115], v[30:31], v[18:19]
	v_pk_fma_f32 v[118:119], v[30:31], v[18:19], v[22:23]
	v_pk_mul_f32 v[4:5], v[4:5], v[24:25]
	v_pk_mul_f32 v[106:107], v[32:33], v[20:21]
	v_pk_mul_f32 v[24:25], v[100:101], v[24:25]
	ds_read_b128 v[98:101], v213 offset:18432
	v_cvt_pk_bf16_f32 v19, v106, v107
	ds_read_b128 v[106:109], v213 offset:19456
	v_pk_fma_f32 v[110:111], v[8:9], v[20:21], v[4:5]
	v_cvt_pk_bf16_f32 v5, v4, v5
	v_cvt_pk_bf16_f32 v3, v10, v11
	v_cvt_pk_bf16_f32 v4, v14, v15
	s_waitcnt lgkmcnt(0)
	v_pk_mul_f32 v[106:107], v[106:107], v[86:87]
	v_cvt_pk_bf16_f32 v2, v12, v13
	v_pk_mul_f32 v[120:121], v[98:99], v[82:83]
	v_pk_mul_f32 v[108:109], v[108:109], v[88:89]
	v_pk_fma_f32 v[98:99], v[98:99], v[82:83], v[106:107]
	v_mfma_f32_32x32x16_bf16 v[2:17], v[26:29], v[2:5], 0
	v_cvt_pk_bf16_f32 v18, v114, v115
	v_mul_f32_e64 v114, v100, v84
	v_mul_f32_e64 v115, v101, v85
	v_fma_f32 v100, v100, v84, v108
	v_fma_f32 v101, v101, v85, v109
	v_pk_add_f32 v[124:125], v[98:99], v[112:113]
	v_pk_add_f32 v[122:123], v[100:101], v[110:111]
	v_cvt_pk_bf16_f32 v101, v108, v109
	v_cvt_pk_bf16_f32 v100, v106, v107
	ds_read_b128 v[106:109], v213 offset:26624
	v_pk_fma_f32 v[116:117], v[32:33], v[20:21], v[24:25]
	v_cvt_pk_bf16_f32 v21, v24, v25
	v_cvt_pk_bf16_f32 v20, v22, v23
	ds_read_b128 v[110:113], v213 offset:27648
	v_cvt_pk_bf16_f32 v99, v114, v115
	v_mfma_f32_32x32x16_bf16 v[18:33], v[26:29], v[18:21], 0
	v_cvt_pk_bf16_f32 v98, v120, v121
	s_waitcnt lgkmcnt(1)
	v_mul_f32_e64 v114, v106, v82
	v_mul_f32_e64 v115, v107, v83
	s_waitcnt lgkmcnt(0)
	v_pk_mul_f32 v[86:87], v[110:111], v[86:87]
	v_pk_mul_f32 v[88:89], v[112:113], v[88:89]
	v_pk_fma_f32 v[82:83], v[106:107], v[82:83], v[86:87]
	v_mfma_f32_32x32x16_bf16 v[2:17], v[102:105], v[98:101], v[2:17]
	v_mul_f32_e64 v98, v108, v84
	v_mul_f32_e64 v99, v109, v85
	v_fma_f32 v84, v108, v84, v88
	v_fma_f32 v85, v109, v85, v89
	v_add_f32_e64 v108, v82, v118
	v_add_f32_e64 v109, v83, v119
	v_cvt_pk_bf16_f32 v83, v98, v99
	v_pk_add_f32 v[106:107], v[84:85], v[116:117]
	v_cvt_pk_bf16_f32 v85, v88, v89
	v_cvt_pk_bf16_f32 v84, v86, v87
	ds_read_b128 v[86:89], v213 offset:38912
	ds_read_b128 v[98:101], v213 offset:20480
	v_cvt_pk_bf16_f32 v82, v114, v115
	s_waitcnt lgkmcnt(0)
	v_pk_mul_f32 v[110:111], v[100:101], v[76:77]
	v_mfma_f32_32x32x16_bf16 v[18:33], v[102:105], v[82:85], v[18:33]
	ds_read_b128 v[82:85], v213 offset:21504
	ds_read_b128 v[102:105], v213 offset:28672
	v_mul_f32_e64 v112, v98, v74
	v_mul_f32_e64 v113, v99, v75
	s_waitcnt lgkmcnt(1)
	v_pk_mul_f32 v[84:85], v[84:85], v[80:81]
	v_pk_mul_f32 v[114:115], v[82:83], v[78:79]
	v_pk_fma_f32 v[82:83], v[100:101], v[76:77], v[84:85]
	v_cvt_pk_bf16_f32 v85, v84, v85
	v_pk_add_f32 v[116:117], v[82:83], v[122:123]
	v_cvt_pk_bf16_f32 v83, v110, v111
	v_cvt_pk_bf16_f32 v84, v114, v115
	v_cvt_pk_bf16_f32 v82, v112, v113
	v_pk_fma_f32 v[98:99], v[98:99], v[74:75], v[114:115]
	s_waitcnt lgkmcnt(0)
	v_pk_mul_f32 v[112:113], v[102:103], v[74:75]
	v_mfma_f32_32x32x16_bf16 v[2:17], v[86:89], v[82:85], v[2:17]
	ds_read_b128 v[82:85], v213 offset:29696
	v_add_f32_e64 v118, v98, v124
	v_add_f32_e64 v119, v99, v125
	v_mul_f32_e64 v110, v104, v76
	v_mul_f32_e64 v111, v105, v77
	ds_read_b128 v[98:101], v213 offset:39936
	s_waitcnt lgkmcnt(1)
	v_pk_mul_f32 v[78:79], v[82:83], v[78:79]
	v_pk_mul_f32 v[80:81], v[84:85], v[80:81]
	v_pk_fma_f32 v[74:75], v[102:103], v[74:75], v[78:79]
	v_pk_fma_f32 v[76:77], v[104:105], v[76:77], v[80:81]
	v_pk_add_f32 v[104:105], v[74:75], v[108:109]
	v_pk_add_f32 v[102:103], v[76:77], v[106:107]
	v_cvt_pk_bf16_f32 v77, v80, v81
	v_cvt_pk_bf16_f32 v76, v78, v79
	ds_read_b128 v[78:81], v213 offset:22528
	ds_read_b128 v[82:85], v213 offset:23552
	v_cvt_pk_bf16_f32 v75, v110, v111
	v_cvt_pk_bf16_f32 v74, v112, v113
	s_waitcnt lgkmcnt(0)
	v_pk_mul_f32 v[82:83], v[82:83], v[70:71]
	v_mfma_f32_32x32x16_bf16 v[18:33], v[86:89], v[74:77], v[18:33]
	v_mul_f32_e64 v74, v80, v68
	v_mul_f32_e64 v75, v81, v69
	v_mul_f32_e64 v76, v84, v72
	v_mul_f32_e64 v77, v85, v73
	v_mul_f32_e64 v86, v78, v66
	v_mul_f32_e64 v87, v79, v67
	v_pk_fma_f32 v[80:81], v[80:81], v[68:69], v[76:77]
	v_pk_fma_f32 v[78:79], v[78:79], v[66:67], v[82:83]
	v_cvt_pk_bf16_f32 v75, v74, v75
	v_pk_add_f32 v[88:89], v[80:81], v[116:117]
	v_pk_add_f32 v[106:107], v[78:79], v[118:119]
	ds_read_b128 v[78:81], v213 offset:30720
	v_cvt_pk_bf16_f32 v77, v76, v77
	v_cvt_pk_bf16_f32 v76, v82, v83
	ds_read_b128 v[82:85], v213 offset:31744
	v_cvt_pk_bf16_f32 v74, v86, v87
	s_waitcnt lgkmcnt(0)
	v_pk_mul_f32 v[72:73], v[84:85], v[72:73]
	v_mfma_f32_32x32x16_bf16 v[2:17], v[98:101], v[74:77], v[2:17]
	v_mul_f32_e64 v74, v80, v68
	v_mul_f32_e64 v75, v81, v69
	v_fma_f32 v68, v80, v68, v72
	v_fma_f32 v69, v81, v69, v73
	v_mul_f32_e64 v70, v82, v70
	v_mul_f32_e64 v71, v83, v71
	v_pk_add_f32 v[84:85], v[68:69], v[102:103]
	v_cvt_pk_bf16_f32 v69, v72, v73
	v_pk_mov_b32 v[72:73], v[96:97], v[94:95] op_sel:[1,0]
	v_mov_b32_e32 v97, v95
	v_pk_add_f32 v[72:73], v[72:73], v[96:97]
	v_pk_mul_f32 v[76:77], v[78:79], v[66:67]
	v_pk_fma_f32 v[66:67], v[78:79], v[66:67], v[70:71]
	v_pk_add_f32 v[72:73], v[72:73], v[72:73] op_sel:[0,1] op_sel_hi:[1,0]
	v_pk_add_f32 v[86:87], v[66:67], v[104:105]
	v_mov_b32_e32 v66, v72
	s_nop 1
	v_permlane32_swap_b32_e32 v72, v66
	v_add_f32_e32 v66, v72, v66
	v_cvt_pk_bf16_f32 v67, v74, v75
	v_rcp_f32_e32 v74, v66
	v_cvt_pk_bf16_f32 v68, v70, v71
	v_cvt_pk_bf16_f32 v66, v76, v77
	v_pk_mul_f32 v[70:71], v[46:47], v[74:75] op_sel_hi:[1,0]
	s_nop 0
	v_mfma_f32_32x32x16_bf16 v[18:33], v[98:101], v[66:69], v[18:33]
	v_mul_f32_e64 v66, v42, v74
	v_mul_f32_e64 v67, v43, v74
	v_pk_mov_b32 v[42:43], v[92:93], v[90:91] op_sel:[1,0]
	v_mov_b32_e32 v93, v91
	v_pk_add_f32 v[42:43], v[42:43], v[92:93]
	v_pk_mul_f32 v[68:69], v[44:45], v[74:75] op_sel_hi:[1,0]
	v_pk_add_f32 v[42:43], v[42:43], v[42:43] op_sel:[0,1] op_sel_hi:[1,0]
	v_pk_mov_b32 v[44:45], v[106:107], v[88:89] op_sel:[1,0]
	v_mov_b32_e32 v43, v42
	s_nop 1
	v_permlane32_swap_b32_e32 v42, v43
	v_add_f32_e32 v42, v42, v43
	v_rcp_f32_e32 v42, v42
	v_mov_b32_e32 v107, v89
	v_pk_add_f32 v[44:45], v[44:45], v[106:107]
	v_pk_mul_f32 v[72:73], v[48:49], v[74:75] op_sel_hi:[1,0]
	v_pk_add_f32 v[44:45], v[44:45], v[44:45] op_sel:[0,1] op_sel_hi:[1,0]
	v_pk_mul_f32 v[36:37], v[36:37], v[74:75] op_sel_hi:[1,0]
	v_pk_mul_f32 v[38:39], v[38:39], v[74:75] op_sel_hi:[1,0]
	v_pk_mul_f32 v[40:41], v[40:41], v[74:75] op_sel_hi:[1,0]
	v_pk_mul_f32 v[34:35], v[34:35], v[74:75] op_sel_hi:[1,0]
	v_pk_mul_f32 v[74:75], v[58:59], v[42:43] op_sel_hi:[1,0]
	v_pk_mul_f32 v[78:79], v[60:61], v[42:43] op_sel_hi:[1,0]
	v_pk_mul_f32 v[80:81], v[62:63], v[42:43] op_sel_hi:[1,0]
	v_pk_mul_f32 v[82:83], v[64:65], v[42:43] op_sel_hi:[1,0]
	v_pk_mul_f32 v[92:93], v[52:53], v[42:43] op_sel_hi:[1,0]
	v_mov_b32_e32 v43, v44
	s_nop 1
	v_permlane32_swap_b32_e32 v44, v43
	v_add_f32_e32 v43, v44, v43
	v_rcp_f32_e32 v76, v43
	v_pk_mul_f32 v[96:97], v[54:55], v[42:43] op_sel_hi:[1,0]
	v_pk_mul_f32 v[94:95], v[56:57], v[42:43] op_sel_hi:[1,0]
	v_pk_mul_f32 v[98:99], v[50:51], v[42:43] op_sel_hi:[1,0]
	v_pk_mul_f32 v[100:101], v[4:5], v[76:77] op_sel_hi:[1,0]
	v_pk_mov_b32 v[4:5], v[86:87], v[84:85] op_sel:[1,0]
	v_mov_b32_e32 v87, v85
	v_pk_add_f32 v[4:5], v[4:5], v[86:87]
	v_pk_mul_f32 v[102:103], v[6:7], v[76:77] op_sel_hi:[1,0]
	v_pk_add_f32 v[104:105], v[4:5], v[4:5] op_sel:[0,1] op_sel_hi:[1,0]
	v_cvt_pk_bf16_f32 v7, v40, v41
	ds_read_b128 v[84:87], v150 offset:52224
	ds_read_b128 v[50:53], v150 offset:35840
	ds_read_b128 v[54:57], v150 offset:36864
	ds_read_b128 v[58:61], v150 offset:37888
	ds_read_b128 v[62:65], v150 offset:38912
	v_cvt_pk_bf16_f32 v6, v38, v39
	v_cvt_pk_bf16_f32 v5, v36, v37
	v_cvt_pk_bf16_f32 v4, v34, v35
	ds_read_b128 v[88:91], v150 offset:53248
	ds_read_b128 v[34:37], v150 offset:39936
	ds_read_b128 v[38:41], v150 offset:40960
	ds_read_b128 v[42:45], v150 offset:41984
	ds_read_b128 v[46:49], v150 offset:43008
	v_cvt_pk_bf16_f32 v95, v94, v95
	v_cvt_pk_bf16_f32 v94, v96, v97
	v_cvt_pk_bf16_f32 v93, v92, v93
	v_cvt_pk_bf16_f32 v92, v98, v99
	s_waitcnt lgkmcnt(5)
	v_mfma_f32_32x32x16_bf16 v[50:65], v[84:87], v[4:7], v[50:65]
	v_mul_f32_e64 v10, v10, v76
	v_mul_f32_e64 v11, v11, v76
	v_mul_f32_e64 v12, v12, v76
	v_mul_f32_e64 v13, v13, v76
	v_mul_f32_e64 v8, v8, v76
	v_mul_f32_e64 v9, v9, v76
	v_mov_b32_e32 v77, v104
	s_nop 1
	v_permlane32_swap_b32_e32 v104, v77
	v_cvt_pk_bf16_f32 v73, v72, v73
	s_waitcnt lgkmcnt(0)
	v_mfma_f32_32x32x16_bf16 v[34:49], v[84:87], v[92:95], v[34:49]
	v_cvt_pk_bf16_f32 v72, v70, v71
	v_cvt_pk_bf16_f32 v70, v66, v67
	v_add_f32_e32 v66, v104, v77
	v_cvt_pk_bf16_f32 v71, v68, v69
	v_rcp_f32_e32 v104, v66
	v_cvt_pk_bf16_f32 v69, v82, v83
	v_cvt_pk_bf16_f32 v68, v80, v81
	v_cvt_pk_bf16_f32 v67, v78, v79
	v_cvt_pk_bf16_f32 v66, v74, v75
	ds_read_b128 v[78:81], v150 offset:54272
	v_mfma_f32_32x32x16_bf16 v[50:65], v[88:91], v[70:73], v[50:65]
	v_mul_f32_e64 v2, v2, v76
	v_mul_f32_e64 v3, v3, v76
	v_mul_f32_e64 v20, v20, v104
	v_mul_f32_e64 v21, v21, v104
	v_cvt_pk_bf16_f32 v85, v8, v9
	v_cvt_pk_bf16_f32 v82, v2, v3
	v_pk_mul_f32 v[2:3], v[22:23], v[104:105] op_sel_hi:[1,0]
	v_pk_mul_f32 v[8:9], v[24:25], v[104:105] op_sel_hi:[1,0]
	v_pk_mul_f32 v[18:19], v[18:19], v[104:105] op_sel_hi:[1,0]
	v_mfma_f32_32x32x16_bf16 v[34:49], v[88:91], v[66:69], v[34:49]
	v_cvt_pk_bf16_f32 v84, v102, v103
	v_cvt_pk_bf16_f32 v83, v100, v101
	ds_read_b128 v[86:89], v150 offset:55296
	v_cvt_pk_bf16_f32 v99, v8, v9
	v_cvt_pk_bf16_f32 v98, v2, v3
	v_cvt_pk_bf16_f32 v97, v20, v21
	v_cvt_pk_bf16_f32 v96, v18, v19
	s_waitcnt lgkmcnt(1)
	v_mfma_f32_32x32x16_bf16 v[50:65], v[78:81], v[82:85], v[50:65]
	v_mul_f32_e64 v2, v14, v76
	v_mul_f32_e64 v3, v15, v76
	v_mul_f32_e64 v8, v16, v76
	v_mul_f32_e64 v9, v17, v76
	v_mul_f32_e64 v14, v26, v104
	v_mul_f32_e64 v15, v27, v104
	v_cvt_pk_bf16_f32 v77, v8, v9
	v_cvt_pk_bf16_f32 v76, v2, v3
	v_cvt_pk_bf16_f32 v74, v10, v11
	v_pk_mul_f32 v[2:3], v[28:29], v[104:105] op_sel_hi:[1,0]
	v_mfma_f32_32x32x16_bf16 v[34:49], v[78:81], v[96:99], v[34:49]
	v_mul_f32_e64 v8, v30, v104
	v_mul_f32_e64 v9, v31, v104
	v_mul_f32_e64 v10, v32, v104
	v_mul_f32_e64 v11, v33, v104
	v_cvt_pk_bf16_f32 v75, v12, v13
	v_cvt_pk_bf16_f32 v81, v10, v11
	v_cvt_pk_bf16_f32 v80, v8, v9
	v_cvt_pk_bf16_f32 v79, v2, v3
	v_cvt_pk_bf16_f32 v78, v14, v15
	s_waitcnt lgkmcnt(0)
	v_mfma_f32_32x32x16_bf16 v[50:65], v[86:89], v[74:77], v[50:65]
	v_mfma_f32_32x32x16_bf16 v[34:49], v[86:89], v[78:81], v[34:49]
	ds_read_b128 v[86:89], v150 offset:56320
	ds_read_b128 v[18:21], v150 offset:44032
	ds_read_b128 v[22:25], v150 offset:45056
	ds_read_b128 v[26:29], v150 offset:46080
	ds_read_b128 v[30:33], v150 offset:47104
	ds_read_b128 v[100:103], v150 offset:57344
	s_waitcnt lgkmcnt(1)
	v_mfma_f32_32x32x16_bf16 v[18:33], v[86:89], v[4:7], v[18:33]
	ds_read_b128 v[2:5], v150 offset:48128
	ds_read_b128 v[6:9], v150 offset:49152
	ds_read_b128 v[10:13], v150 offset:50176
	ds_read_b128 v[14:17], v150 offset:51200
	s_waitcnt lgkmcnt(0)
	v_mfma_f32_32x32x16_bf16 v[2:17], v[86:89], v[92:95], v[2:17]
	v_mfma_f32_32x32x16_bf16 v[18:33], v[100:103], v[70:73], v[18:33]
	v_mfma_f32_32x32x16_bf16 v[2:17], v[100:103], v[66:69], v[2:17]
	ds_read_b128 v[66:69], v150 offset:58368
	ds_read_b128 v[70:73], v150 offset:59392
	s_waitcnt lgkmcnt(1)
	v_mfma_f32_32x32x16_bf16 v[18:33], v[66:69], v[82:85], v[18:33]
	v_mfma_f32_32x32x16_bf16 v[2:17], v[66:69], v[96:99], v[2:17]
	s_waitcnt lgkmcnt(0)
	v_mfma_f32_32x32x16_bf16 v[18:33], v[70:73], v[74:77], v[18:33]
	v_mfma_f32_32x32x16_bf16 v[2:17], v[70:73], v[78:81], v[2:17]
	s_nop 10
	v_mul_f32_e64 v66, v22, v22
	v_mul_f32_e64 v67, v23, v23
	v_mul_f32_e64 v68, v30, v30
	v_mul_f32_e64 v69, v31, v31
	v_mul_f32_e64 v70, v24, v24
	v_mul_f32_e64 v71, v25, v25
	v_pk_mul_f32 v[72:73], v[32:33], v[32:33]
	v_pk_mul_f32 v[74:75], v[20:21], v[20:21]
	v_pk_mul_f32 v[76:77], v[28:29], v[28:29]
	v_pk_mul_f32 v[78:79], v[26:27], v[26:27]
	v_pk_mul_f32 v[80:81], v[18:19], v[18:19]
	v_pk_fma_f32 v[78:79], v[58:59], v[58:59], v[78:79]
	v_pk_fma_f32 v[76:77], v[60:61], v[60:61], v[76:77]
	v_pk_fma_f32 v[74:75], v[52:53], v[52:53], v[74:75]
	v_pk_fma_f32 v[72:73], v[64:65], v[64:65], v[72:73]
	v_pk_fma_f32 v[70:71], v[56:57], v[56:57], v[70:71]
	v_pk_fma_f32 v[68:69], v[62:63], v[62:63], v[68:69]
	v_pk_fma_f32 v[66:67], v[54:55], v[54:55], v[66:67]
	v_pk_fma_f32 v[80:81], v[50:51], v[50:51], v[80:81]
	v_pk_add_f32 v[66:67], v[66:67], v[68:69]
	v_pk_add_f32 v[68:69], v[70:71], v[72:73]
	v_pk_add_f32 v[70:71], v[74:75], v[76:77]
	v_pk_add_f32 v[72:73], v[80:81], v[78:79]
	v_pk_add_f32 v[68:69], v[70:71], v[68:69]
	v_pk_add_f32 v[66:67], v[72:73], v[66:67]
	v_pk_mul_f32 v[72:73], v[14:15], v[14:15]
	v_pk_mov_b32 v[70:71], v[66:67], v[68:69] op_sel:[1,0]
	v_mov_b32_e32 v67, v69
	v_pk_add_f32 v[66:67], v[70:71], v[66:67]
	v_pk_mul_f32 v[70:71], v[6:7], v[6:7]
	v_pk_mul_f32 v[74:75], v[8:9], v[8:9]
	v_pk_mul_f32 v[76:77], v[16:17], v[16:17]
	v_pk_mul_f32 v[78:79], v[4:5], v[4:5]
	v_pk_mul_f32 v[80:81], v[12:13], v[12:13]
	v_pk_mul_f32 v[82:83], v[10:11], v[10:11]
	v_pk_mul_f32 v[84:85], v[2:3], v[2:3]
	v_pk_fma_f32 v[82:83], v[42:43], v[42:43], v[82:83]
	v_pk_fma_f32 v[80:81], v[44:45], v[44:45], v[80:81]
	v_pk_fma_f32 v[78:79], v[36:37], v[36:37], v[78:79]
	v_pk_fma_f32 v[76:77], v[48:49], v[48:49], v[76:77]
	v_pk_fma_f32 v[74:75], v[40:41], v[40:41], v[74:75]
	v_pk_fma_f32 v[72:73], v[46:47], v[46:47], v[72:73]
	v_pk_fma_f32 v[70:71], v[38:39], v[38:39], v[70:71]
	v_pk_fma_f32 v[84:85], v[34:35], v[34:35], v[84:85]
	v_pk_add_f32 v[70:71], v[70:71], v[72:73]
	v_pk_add_f32 v[72:73], v[74:75], v[76:77]
	v_pk_add_f32 v[74:75], v[78:79], v[80:81]
	v_pk_add_f32 v[76:77], v[84:85], v[82:83]
	v_pk_add_f32 v[72:73], v[74:75], v[72:73]
	v_pk_add_f32 v[70:71], v[76:77], v[70:71]
	v_pk_add_f32 v[66:67], v[66:67], v[66:67] op_sel:[0,1] op_sel_hi:[1,0]
	v_pk_mov_b32 v[74:75], v[70:71], v[72:73] op_sel:[1,0]
	v_mov_b32_e32 v71, v73
	v_pk_add_f32 v[70:71], v[74:75], v[70:71]
	v_mov_b32_e32 v69, v66
	v_pk_add_f32 v[70:71], v[70:71], v[70:71] op_sel:[0,1] op_sel_hi:[1,0]
	s_nop 0
	v_permlane32_swap_b32_e32 v66, v69
	v_mov_b32_e32 v68, v70
	s_nop 1
	v_permlane32_swap_b32_e32 v70, v68
	v_mov_b32_e32 v71, v66
	v_pk_add_f32 v[66:67], v[70:71], v[68:69]
	s_nop 0
	v_pk_fma_f32 v[66:67], v[66:67], s[0:1], v[152:153] op_sel_hi:[1,0,0]
	s_mov_b32 s1, 0x800000
	v_mul_f32_e32 v68, 0x4b800000, v67
	v_cmp_gt_f32_e32 vcc, s1, v67
	s_nop 1
	v_cndmask_b32_e32 v67, v67, v68, vcc
	v_rsq_f32_e32 v67, v67
	s_nop 0
	v_mul_f32_e32 v68, 0x45800000, v67
	v_cndmask_b32_e32 v68, v67, v68, vcc
	v_pk_mul_f32 v[158:159], v[50:51], v[68:69] op_sel_hi:[1,0]
	v_pk_mul_f32 v[50:51], v[18:19], v[68:69] op_sel_hi:[1,0]
	v_mul_f32_e32 v18, 0x4b800000, v66
	v_cmp_gt_f32_e32 vcc, s1, v66
	v_pk_mul_f32 v[80:81], v[60:61], v[68:69] op_sel_hi:[1,0]
	v_pk_mul_f32 v[60:61], v[28:29], v[68:69] op_sel_hi:[1,0]
	v_cndmask_b32_e32 v18, v66, v18, vcc
	v_rsq_f32_e32 v18, v18
	v_pk_mul_f32 v[78:79], v[58:59], v[68:69] op_sel_hi:[1,0]
	v_pk_mul_f32 v[160:161], v[52:53], v[68:69] op_sel_hi:[1,0]
	v_pk_mul_f32 v[82:83], v[54:55], v[68:69] op_sel_hi:[1,0]
	v_mul_f32_e32 v19, 0x45800000, v18
	v_cndmask_b32_e32 v28, v18, v19, vcc
	v_pk_mul_f32 v[168:169], v[56:57], v[68:69] op_sel_hi:[1,0]
	v_pk_mul_f32 v[58:59], v[26:27], v[68:69] op_sel_hi:[1,0]
	v_pk_mul_f32 v[52:53], v[20:21], v[68:69] op_sel_hi:[1,0]
	v_pk_mul_f32 v[54:55], v[22:23], v[68:69] op_sel_hi:[1,0]
	v_pk_mul_f32 v[56:57], v[24:25], v[68:69] op_sel_hi:[1,0]
	v_pk_mul_f32 v[18:19], v[42:43], v[28:29] op_sel_hi:[1,0]
	v_pk_mul_f32 v[20:21], v[44:45], v[28:29] op_sel_hi:[1,0]
	v_pk_mul_f32 v[22:23], v[46:47], v[28:29] op_sel_hi:[1,0]
	v_pk_mul_f32 v[26:27], v[48:49], v[28:29] op_sel_hi:[1,0]
	v_pk_mul_f32 v[162:163], v[34:35], v[28:29] op_sel_hi:[1,0]
	v_pk_mul_f32 v[164:165], v[36:37], v[28:29] op_sel_hi:[1,0]
	v_pk_mul_f32 v[166:167], v[38:39], v[28:29] op_sel_hi:[1,0]
	v_pk_mul_f32 v[24:25], v[40:41], v[28:29] op_sel_hi:[1,0]
	v_pk_mul_f32 v[104:105], v[2:3], v[28:29] op_sel_hi:[1,0]
	v_pk_mul_f32 v[112:113], v[4:5], v[28:29] op_sel_hi:[1,0]
	ds_read_b128 v[2:5], v150 offset:60416
	ds_read_b128 v[34:37], v174 offset:32768
	ds_read_b128 v[38:41], v174 offset:32800
	ds_read_b128 v[42:45], v174 offset:32832
	ds_read_b128 v[46:49], v174 offset:32864
	v_cvt_pk_bf16_f32 v129, v168, v169
	v_cvt_pk_bf16_f32 v128, v82, v83
	v_cvt_pk_bf16_f32 v127, v160, v161
	v_cvt_pk_bf16_f32 v126, v158, v159
	v_cvt_pk_bf16_f32 v137, v24, v25
	v_cvt_pk_bf16_f32 v136, v166, v167
	v_cvt_pk_bf16_f32 v135, v164, v165
	s_waitcnt lgkmcnt(0)
	v_mfma_f32_32x32x16_bf16 v[86:101], v[2:5], v[126:129], v[34:49]
	v_cvt_pk_bf16_f32 v134, v162, v163
	v_mul_f32_e64 v84, v62, v68
	v_mul_f32_e64 v85, v63, v68
	v_mul_f32_e64 v170, v64, v68
	v_mul_f32_e64 v171, v65, v68
	v_pk_mul_f32 v[62:63], v[30:31], v[68:69] op_sel_hi:[1,0]
	v_pk_mul_f32 v[64:65], v[32:33], v[68:69] op_sel_hi:[1,0]
	v_pk_mul_f32 v[116:117], v[6:7], v[28:29] op_sel_hi:[1,0]
	v_pk_mul_f32 v[154:155], v[8:9], v[28:29] op_sel_hi:[1,0]
	v_mfma_f32_32x32x16_bf16 v[34:49], v[2:5], v[134:137], v[34:49]
	ds_read_b128 v[6:9], v150 offset:61440
	ds_read_b128 v[66:69], v174 offset:32896
	ds_read_b128 v[106:109], v150 offset:64512
	v_cvt_pk_bf16_f32 v125, v170, v171
	v_cvt_pk_bf16_f32 v124, v84, v85
	v_cvt_pk_bf16_f32 v123, v80, v81
	v_cvt_pk_bf16_f32 v122, v78, v79
	v_cvt_pk_bf16_f32 v149, v26, v27
	v_cvt_pk_bf16_f32 v148, v22, v23
	v_cvt_pk_bf16_f32 v147, v20, v21
	v_cvt_pk_bf16_f32 v146, v18, v19
	s_waitcnt lgkmcnt(2)
	v_mfma_f32_32x32x16_bf16 v[86:101], v[6:9], v[122:125], v[86:101]
	v_mul_f32_e64 v102, v10, v28
	v_mul_f32_e64 v103, v11, v28
	v_mul_f32_e64 v110, v12, v28
	v_mul_f32_e64 v111, v13, v28
	v_mul_f32_e64 v114, v14, v28
	v_mul_f32_e64 v115, v15, v28
	v_pk_mul_f32 v[156:157], v[16:17], v[28:29] op_sel_hi:[1,0]
	ds_read_b128 v[176:179], v174 offset:33536
	ds_read_b128 v[180:183], v174 offset:33568
	ds_read_b128 v[184:187], v174 offset:33600
	ds_read_b128 v[28:31], v174 offset:33632
	ds_read_b128 v[188:191], v174 offset:33792
	ds_read_b128 v[192:195], v174 offset:33824
	ds_read_b128 v[196:199], v174 offset:33856
	ds_read_b128 v[200:203], v174 offset:33888
	ds_read_b128 v[204:207], v150 offset:62464
	v_cvt_pk_bf16_f32 v133, v56, v57
	v_mfma_f32_32x32x16_bf16 v[34:49], v[6:9], v[146:149], v[34:49]
	v_cvt_pk_bf16_f32 v132, v54, v55
	v_cvt_pk_bf16_f32 v131, v52, v53
	v_cvt_pk_bf16_f32 v130, v50, v51
	ds_read_b128 v[70:73], v174 offset:33664
	ds_read_b128 v[74:77], v174 offset:33920
	ds_read_b128 v[208:211], v150 offset:63488
	v_cvt_pk_bf16_f32 v145, v154, v155
	v_cvt_pk_bf16_f32 v144, v116, v117
	v_cvt_pk_bf16_f32 v143, v112, v113
	v_cvt_pk_bf16_f32 v142, v104, v105
	s_waitcnt lgkmcnt(3)
	v_mfma_f32_32x32x16_bf16 v[86:101], v[204:207], v[130:133], v[86:101]
	v_cvt_pk_bf16_f32 v121, v64, v65
	v_cvt_pk_bf16_f32 v120, v62, v63
	v_cvt_pk_bf16_f32 v119, v60, v61
	v_cvt_pk_bf16_f32 v118, v58, v59
	v_cvt_pk_bf16_f32 v141, v156, v157
	v_cvt_pk_bf16_f32 v140, v114, v115
	v_cvt_pk_bf16_f32 v139, v110, v111
	v_mfma_f32_32x32x16_bf16 v[34:49], v[204:207], v[142:145], v[34:49]
	v_cvt_pk_bf16_f32 v138, v102, v103
	v_fma_f32 v16, v30, v170, v202
	v_fma_f32 v17, v31, v171, v203
	v_fma_f32 v14, v28, v84, v200
	v_fma_f32 v15, v29, v85, v201
	v_pk_fma_f32 v[12:13], v[186:187], v[80:81], v[198:199]
	v_pk_fma_f32 v[10:11], v[184:185], v[78:79], v[196:197]
	v_pk_fma_f32 v[8:9], v[182:183], v[168:169], v[194:195]
	s_waitcnt lgkmcnt(0)
	v_mfma_f32_32x32x16_bf16 v[86:101], v[208:211], v[118:121], v[86:101]
	v_fma_f32 v6, v180, v82, v192
	v_fma_f32 v7, v181, v83, v193
	ds_read_b128 v[78:81], v174 offset:33760
	ds_read_b128 v[82:85], v174 offset:33248
	v_fma_f32 v4, v178, v160, v190
	v_fma_f32 v5, v179, v161, v191
	v_pk_fma_f32 v[2:3], v[176:177], v[158:159], v[188:189]
	v_pk_fma_f32 v[32:33], v[30:31], v[26:27], v[202:203]
	v_pk_fma_f32 v[30:31], v[28:29], v[22:23], v[200:201]
	v_pk_fma_f32 v[28:29], v[186:187], v[20:21], v[198:199]
	v_pk_fma_f32 v[26:27], v[184:185], v[18:19], v[196:197]
	v_pk_fma_f32 v[24:25], v[182:183], v[24:25], v[194:195]
	v_pk_fma_f32 v[22:23], v[180:181], v[166:167], v[192:193]
	v_pk_fma_f32 v[20:21], v[178:179], v[164:165], v[190:191]
	v_pk_fma_f32 v[18:19], v[176:177], v[162:163], v[188:189]
	ds_read_b128 v[158:161], v174 offset:33696
	ds_read_b128 v[162:165], v174 offset:33728
	ds_read_b128 v[166:169], v174 offset:33952
	ds_read_b128 v[176:179], v174 offset:33984
	ds_read_b128 v[180:183], v174 offset:34016
	ds_read_b128 v[184:187], v212 offset:11264
	v_mfma_f32_32x32x16_bf16 v[34:49], v[208:211], v[138:141], v[34:49]
	v_cvt_pk_bf16_f32 v86, v86, v87
	v_cvt_pk_bf16_f32 v87, v88, v89
	v_cvt_pk_bf16_f32 v88, v90, v91
	v_cvt_pk_bf16_f32 v89, v92, v93
	ds_read_b128 v[90:93], v212 offset:12288
	v_pk_max_i16 v86, v86, 0
	v_pk_max_i16 v87, v87, 0
	v_pk_max_i16 v88, v88, 0
	v_pk_max_i16 v89, v89, 0
	s_nop 1
	s_nop 5
	v_cvt_pk_bf16_f32 v188, v34, v35
	v_cvt_pk_bf16_f32 v189, v36, v37
	v_cvt_pk_bf16_f32 v190, v38, v39
	v_cvt_pk_bf16_f32 v191, v40, v41
	s_waitcnt lgkmcnt(1)
	v_mfma_f32_32x32x16_bf16 v[2:17], v[184:187], v[86:89], v[2:17]
	v_pk_max_i16 v188, v188, 0
	v_pk_max_i16 v189, v189, 0
	v_pk_max_i16 v190, v190, 0
	v_pk_max_i16 v191, v191, 0
	s_nop 1
	v_cvt_pk_bf16_f32 v94, v94, v95
	v_cvt_pk_bf16_f32 v95, v96, v97
	v_cvt_pk_bf16_f32 v96, v98, v99
	v_cvt_pk_bf16_f32 v97, v100, v101
	v_cvt_pk_bf16_f32 v98, v42, v43
	v_cvt_pk_bf16_f32 v99, v44, v45
	v_mfma_f32_32x32x16_bf16 v[18:33], v[184:187], v[188:191], v[18:33]
	ds_read_b128 v[184:187], v212 offset:19456
	v_cvt_pk_bf16_f32 v100, v46, v47
	v_cvt_pk_bf16_f32 v101, v48, v49
	v_fma_f32 v64, v80, v64, v182
	v_fma_f32 v65, v81, v65, v183
	v_pk_fma_f32 v[62:63], v[78:79], v[62:63], v[180:181]
	v_pk_fma_f32 v[60:61], v[164:165], v[60:61], v[178:179]
	v_pk_fma_f32 v[58:59], v[162:163], v[58:59], v[176:177]
	v_pk_max_i16 v94, v94, 0
	v_pk_max_i16 v95, v95, 0
	v_pk_max_i16 v96, v96, 0
	v_pk_max_i16 v97, v97, 0
	s_nop 1
	v_pk_max_i16 v98, v98, 0
	v_pk_max_i16 v99, v99, 0
	v_pk_max_i16 v100, v100, 0
	v_pk_max_i16 v101, v101, 0
	s_nop 1
	v_pk_fma_f32 v[56:57], v[160:161], v[56:57], v[168:169]
	s_waitcnt lgkmcnt(1)
	v_mfma_f32_32x32x16_bf16 v[2:17], v[90:93], v[94:97], v[2:17]
	v_fma_f32 v54, v158, v54, v166
	v_fma_f32 v55, v159, v55, v167
	v_fma_f32 v52, v72, v52, v76
	v_fma_f32 v53, v73, v53, v77
	v_fma_f32 v50, v70, v50, v74
	v_fma_f32 v51, v71, v51, v75
	v_pk_fma_f32 v[48:49], v[80:81], v[156:157], v[182:183]
	v_pk_fma_f32 v[46:47], v[78:79], v[114:115], v[180:181]
	v_pk_fma_f32 v[44:45], v[164:165], v[110:111], v[178:179]
	v_pk_fma_f32 v[42:43], v[162:163], v[102:103], v[176:177]
	v_mfma_f32_32x32x16_bf16 v[18:33], v[90:93], v[98:101], v[18:33]
	ds_read_b128 v[90:93], v212 offset:20480
	v_fma_f32 v40, v160, v154, v168
	v_fma_f32 v41, v161, v155, v169
	v_fma_f32 v38, v158, v116, v166
	v_fma_f32 v39, v159, v117, v167
	v_pk_fma_f32 v[36:37], v[72:73], v[112:113], v[76:77]
	v_pk_fma_f32 v[34:35], v[70:71], v[104:105], v[74:75]
	s_waitcnt lgkmcnt(1)
	v_mfma_f32_32x32x16_bf16 v[50:65], v[184:187], v[86:89], v[50:65]
	ds_read_b128 v[70:73], v174 offset:32928
	ds_read_b128 v[74:77], v174 offset:32960
	ds_read_b128 v[78:81], v174 offset:32992
	ds_read_b128 v[86:89], v174 offset:33024
	ds_read_b128 v[110:113], v212 offset:1024
	v_mfma_f32_32x32x16_bf16 v[34:49], v[184:187], v[188:191], v[34:49]
	s_waitcnt lgkmcnt(5)
	v_mfma_f32_32x32x16_bf16 v[50:65], v[90:93], v[94:97], v[50:65]
	v_mfma_f32_32x32x16_bf16 v[34:49], v[90:93], v[98:101], v[34:49]
	s_waitcnt lgkmcnt(2)
	v_mfma_f32_32x32x16_bf16 v[90:105], v[106:109], v[126:129], v[66:81]
	v_mfma_f32_32x32x16_bf16 v[66:81], v[106:109], v[134:137], v[66:81]
	ds_read_b128 v[106:109], v212 offset:0
	s_waitcnt lgkmcnt(0)
	v_mfma_f32_32x32x16_bf16 v[90:105], v[106:109], v[122:125], v[90:105]
	v_mfma_f32_32x32x16_bf16 v[66:81], v[106:109], v[146:149], v[66:81]
	ds_read_b128 v[106:109], v212 offset:2048
	v_mfma_f32_32x32x16_bf16 v[90:105], v[110:113], v[130:133], v[90:105]
	v_mfma_f32_32x32x16_bf16 v[66:81], v[110:113], v[142:145], v[66:81]
	ds_read_b128 v[110:113], v212 offset:13312
	s_waitcnt lgkmcnt(1)
	v_mfma_f32_32x32x16_bf16 v[90:105], v[106:109], v[118:121], v[90:105]
	v_mfma_f32_32x32x16_bf16 v[66:81], v[106:109], v[138:141], v[66:81]
	s_nop 10
	v_cvt_pk_bf16_f32 v90, v90, v91
	v_cvt_pk_bf16_f32 v91, v92, v93
	v_cvt_pk_bf16_f32 v92, v94, v95
	v_cvt_pk_bf16_f32 v94, v98, v99
	v_cvt_pk_bf16_f32 v95, v100, v101
	ds_read_b128 v[98:101], v212 offset:21504
	v_cvt_pk_bf16_f32 v66, v66, v67
	v_cvt_pk_bf16_f32 v67, v68, v69
	v_cvt_pk_bf16_f32 v68, v70, v71
	v_cvt_pk_bf16_f32 v93, v96, v97
	v_cvt_pk_bf16_f32 v69, v72, v73
	ds_read_b128 v[70:73], v212 offset:14336
	v_pk_max_i16 v90, v90, 0
	v_pk_max_i16 v91, v91, 0
	v_pk_max_i16 v92, v92, 0
	v_pk_max_i16 v93, v93, 0
	s_nop 1
	v_pk_max_i16 v66, v66, 0
	v_pk_max_i16 v67, v67, 0
	v_pk_max_i16 v68, v68, 0
	v_pk_max_i16 v69, v69, 0
	s_nop 1
	v_cvt_pk_bf16_f32 v96, v102, v103
	s_waitcnt lgkmcnt(2)
	v_mfma_f32_32x32x16_bf16 v[2:17], v[110:113], v[90:93], v[2:17]
	v_cvt_pk_bf16_f32 v97, v104, v105
	v_cvt_pk_bf16_f32 v74, v74, v75
	v_cvt_pk_bf16_f32 v75, v76, v77
	v_cvt_pk_bf16_f32 v76, v78, v79
	v_cvt_pk_bf16_f32 v77, v80, v81
	v_pk_max_i16 v94, v94, 0
	v_pk_max_i16 v95, v95, 0
	v_pk_max_i16 v96, v96, 0
	v_pk_max_i16 v97, v97, 0
	s_nop 1
	v_pk_max_i16 v74, v74, 0
	v_pk_max_i16 v75, v75, 0
	v_pk_max_i16 v76, v76, 0
	v_pk_max_i16 v77, v77, 0
	s_nop 1
	v_mfma_f32_32x32x16_bf16 v[18:33], v[110:113], v[66:69], v[18:33]
	s_waitcnt lgkmcnt(1)
	v_mfma_f32_32x32x16_bf16 v[34:49], v[98:101], v[66:69], v[34:49]
	ds_read_b128 v[66:69], v212 offset:22528
	v_mfma_f32_32x32x16_bf16 v[50:65], v[98:101], v[90:93], v[50:65]
	s_waitcnt lgkmcnt(1)
	v_mfma_f32_32x32x16_bf16 v[2:17], v[70:73], v[94:97], v[2:17]
	v_mfma_f32_32x32x16_bf16 v[18:33], v[70:73], v[74:77], v[18:33]
	ds_read_b128 v[78:81], v212 offset:3072
	s_waitcnt lgkmcnt(1)
	v_mfma_f32_32x32x16_bf16 v[50:65], v[66:69], v[94:97], v[50:65]
	ds_read_b128 v[90:93], v174 offset:33056
	ds_read_b128 v[94:97], v174 offset:33088
	ds_read_b128 v[98:101], v174 offset:33120
	ds_read_b128 v[70:73], v174 offset:33152
	v_mfma_f32_32x32x16_bf16 v[34:49], v[66:69], v[74:77], v[34:49]
	ds_read_b128 v[66:69], v212 offset:4096
	ds_read_b128 v[74:77], v212 offset:5120
	s_waitcnt lgkmcnt(3)
	v_mfma_f32_32x32x16_bf16 v[102:117], v[78:81], v[126:129], v[86:101]
	v_mfma_f32_32x32x16_bf16 v[86:101], v[78:81], v[134:137], v[86:101]
	s_waitcnt lgkmcnt(1)
	v_mfma_f32_32x32x16_bf16 v[86:101], v[66:69], v[146:149], v[86:101]
	v_mfma_f32_32x32x16_bf16 v[102:117], v[66:69], v[122:125], v[102:117]
	ds_read_b128 v[66:69], v212 offset:6144
	s_waitcnt lgkmcnt(1)
	v_mfma_f32_32x32x16_bf16 v[86:101], v[74:77], v[142:145], v[86:101]
	v_mfma_f32_32x32x16_bf16 v[102:117], v[74:77], v[130:133], v[102:117]
	ds_read_b128 v[74:77], v212 offset:15360
	s_waitcnt lgkmcnt(1)
	v_mfma_f32_32x32x16_bf16 v[86:101], v[66:69], v[138:141], v[86:101]
	v_mfma_f32_32x32x16_bf16 v[102:117], v[66:69], v[118:121], v[102:117]
	s_nop 10
	v_cvt_pk_bf16_f32 v78, v86, v87
	v_cvt_pk_bf16_f32 v80, v90, v91
	v_cvt_pk_bf16_f32 v79, v88, v89
	v_cvt_pk_bf16_f32 v81, v92, v93
	ds_read_b128 v[86:89], v212 offset:16384
	ds_read_b128 v[90:93], v212 offset:23552
	v_cvt_pk_bf16_f32 v66, v102, v103
	v_cvt_pk_bf16_f32 v67, v104, v105
	v_cvt_pk_bf16_f32 v68, v106, v107
	v_cvt_pk_bf16_f32 v69, v108, v109
	v_pk_max_i16 v66, v66, 0
	v_pk_max_i16 v67, v67, 0
	v_pk_max_i16 v68, v68, 0
	v_pk_max_i16 v69, v69, 0
	s_nop 1
	v_pk_max_i16 v78, v78, 0
	v_pk_max_i16 v79, v79, 0
	v_pk_max_i16 v80, v80, 0
	v_pk_max_i16 v81, v81, 0
	s_nop 1
	v_cvt_pk_bf16_f32 v94, v94, v95
	s_waitcnt lgkmcnt(2)
	v_mfma_f32_32x32x16_bf16 v[18:33], v[74:77], v[78:81], v[18:33]
	v_cvt_pk_bf16_f32 v95, v96, v97
	v_cvt_pk_bf16_f32 v96, v98, v99
	v_cvt_pk_bf16_f32 v97, v100, v101
	v_pk_max_i16 v94, v94, 0
	v_pk_max_i16 v95, v95, 0
	v_pk_max_i16 v96, v96, 0
	v_pk_max_i16 v97, v97, 0
	s_nop 1
	v_mfma_f32_32x32x16_bf16 v[2:17], v[74:77], v[66:69], v[2:17]
	v_cvt_pk_bf16_f32 v74, v110, v111
	v_cvt_pk_bf16_f32 v75, v112, v113
	v_cvt_pk_bf16_f32 v76, v114, v115
	v_cvt_pk_bf16_f32 v77, v116, v117
	v_pk_max_i16 v74, v74, 0
	v_pk_max_i16 v75, v75, 0
	v_pk_max_i16 v76, v76, 0
	v_pk_max_i16 v77, v77, 0
	s_nop 1
	s_waitcnt lgkmcnt(0)
	v_mfma_f32_32x32x16_bf16 v[50:65], v[90:93], v[66:69], v[50:65]
	ds_read_b128 v[66:69], v212 offset:24576
	v_mfma_f32_32x32x16_bf16 v[34:49], v[90:93], v[78:81], v[34:49]
	ds_read_b128 v[102:105], v212 offset:7168
	v_mfma_f32_32x32x16_bf16 v[2:17], v[86:89], v[74:77], v[2:17]
	s_waitcnt lgkmcnt(1)
	v_mfma_f32_32x32x16_bf16 v[50:65], v[66:69], v[74:77], v[50:65]
	ds_read_b128 v[74:77], v174 offset:33184
	ds_read_b128 v[78:81], v174 offset:33216
	v_mfma_f32_32x32x16_bf16 v[34:49], v[66:69], v[94:97], v[34:49]
	ds_read_b128 v[66:69], v212 offset:8192
	v_mfma_f32_32x32x16_bf16 v[18:33], v[86:89], v[94:97], v[18:33]
	s_waitcnt lgkmcnt(1)
	v_mfma_f32_32x32x16_bf16 v[86:101], v[102:105], v[126:129], v[70:85]
	v_mfma_f32_32x32x16_bf16 v[70:85], v[102:105], v[134:137], v[70:85]
	ds_read_b128 v[102:105], v212 offset:9216
	v_lshlrev_b32_e32 v135, 2, v1
	v_add_u32_e32 v134, v172, v174
	s_waitcnt lgkmcnt(1)
	v_mfma_f32_32x32x16_bf16 v[86:101], v[66:69], v[122:125], v[86:101]
	v_mfma_f32_32x32x16_bf16 v[70:85], v[66:69], v[146:149], v[70:85]
	ds_read_b128 v[66:69], v212 offset:10240
	s_waitcnt lgkmcnt(1)
	v_mfma_f32_32x32x16_bf16 v[86:101], v[102:105], v[130:133], v[86:101]
	v_mfma_f32_32x32x16_bf16 v[70:85], v[102:105], v[142:145], v[70:85]
	ds_read_b128 v[102:105], v212 offset:17408
	s_waitcnt lgkmcnt(1)
	v_mfma_f32_32x32x16_bf16 v[86:101], v[66:69], v[118:121], v[86:101]
	v_mfma_f32_32x32x16_bf16 v[70:85], v[66:69], v[138:141], v[70:85]
	s_nop 10
	v_cvt_pk_bf16_f32 v68, v90, v91
	v_cvt_pk_bf16_f32 v69, v92, v93
	ds_read_b128 v[90:93], v212 offset:25600
	v_cvt_pk_bf16_f32 v66, v86, v87
	v_cvt_pk_bf16_f32 v67, v88, v89
	v_pk_max_i16 v66, v66, 0
	v_pk_max_i16 v67, v67, 0
	v_pk_max_i16 v68, v68, 0
	v_pk_max_i16 v69, v69, 0
	s_nop 1
	v_cvt_pk_bf16_f32 v70, v70, v71
	v_cvt_pk_bf16_f32 v71, v72, v73
	s_waitcnt lgkmcnt(1)
	v_mfma_f32_32x32x16_bf16 v[2:17], v[102:105], v[66:69], v[2:17]
	v_cvt_pk_bf16_f32 v72, v74, v75
	v_cvt_pk_bf16_f32 v73, v76, v77
	ds_read_b128 v[74:77], v212 offset:18432
	v_cvt_pk_bf16_f32 v86, v94, v95
	v_cvt_pk_bf16_f32 v87, v96, v97
	v_cvt_pk_bf16_f32 v88, v98, v99
	s_waitcnt lgkmcnt(1)
	v_mfma_f32_32x32x16_bf16 v[50:65], v[90:93], v[66:69], v[50:65]
	ds_read_b128 v[66:69], v212 offset:26624
	v_cvt_pk_bf16_f32 v89, v100, v101
	v_pk_max_i16 v86, v86, 0
	v_pk_max_i16 v87, v87, 0
	v_pk_max_i16 v88, v88, 0
	v_pk_max_i16 v89, v89, 0
	s_nop 1
	v_pk_max_i16 v70, v70, 0
	v_pk_max_i16 v71, v71, 0
	v_pk_max_i16 v72, v72, 0
	v_pk_max_i16 v73, v73, 0
	s_nop 1
	v_cvt_pk_bf16_f32 v78, v78, v79
	v_cvt_pk_bf16_f32 v79, v80, v81
	s_waitcnt lgkmcnt(1)
	v_mfma_f32_32x32x16_bf16 v[2:17], v[74:77], v[86:89], v[2:17]
	v_cvt_pk_bf16_f32 v80, v82, v83
	v_cvt_pk_bf16_f32 v81, v84, v85
	v_pk_max_i16 v78, v78, 0
	v_pk_max_i16 v79, v79, 0
	v_pk_max_i16 v80, v80, 0
	v_pk_max_i16 v81, v81, 0
	s_nop 1
	s_waitcnt lgkmcnt(0)
	v_mfma_f32_32x32x16_bf16 v[50:65], v[66:69], v[86:89], v[50:65]
	v_mfma_f32_32x32x16_bf16 v[34:49], v[90:93], v[70:73], v[34:49]
	s_nop 10
	v_add_f32_e64 v130, v10, v58
	v_add_f32_e64 v131, v11, v59
	v_add_f32_e64 v132, v12, v60
	v_add_f32_e64 v133, v13, v61
	v_add_f32_e64 v138, v4, v52
	v_add_f32_e64 v139, v5, v53
	v_pk_add_f32 v[140:141], v[16:17], v[64:65]
	v_pk_add_f32 v[142:143], v[8:9], v[56:57]
	v_pk_add_f32 v[144:145], v[14:15], v[62:63]
	v_pk_add_f32 v[146:147], v[6:7], v[54:55]
	v_mfma_f32_32x32x16_bf16 v[18:33], v[102:105], v[70:73], v[18:33]
	ds_read2st64_b32 v[70:71], v135 offset0:133 offset1:134
	v_add_f32_e64 v148, v2, v50
	v_add_f32_e64 v149, v3, v51
	v_add_f32_e64 v144, v146, v144
	v_add_f32_e64 v145, v147, v145
	v_pk_add_f32 v[140:141], v[142:143], v[140:141]
	v_pk_add_f32 v[132:133], v[138:139], v[132:133]
	v_pk_add_f32 v[130:131], v[148:149], v[130:131]
	v_pk_add_f32 v[132:133], v[132:133], v[140:141]
	v_pk_add_f32 v[130:131], v[130:131], v[144:145]
	v_mfma_f32_32x32x16_bf16 v[34:49], v[66:69], v[78:81], v[34:49]
	v_pk_mov_b32 v[138:139], v[130:131], v[132:133] op_sel:[1,0]
	v_mov_b32_e32 v131, v133
	s_waitcnt vmcnt(0) lgkmcnt(0)
	v_mul_f32_e32 v66, v175, v70
	v_pk_add_f32 v[130:131], v[138:139], v[130:131]
	ds_write_b32 v173, v66 offset:512
	v_mul_f32_e32 v66, v175, v71
	v_pk_add_f32 v[130:131], v[130:131], v[130:131] op_sel:[0,1] op_sel_hi:[1,0]
	s_waitcnt lgkmcnt(0)
	ds_read_b128 v[102:105], v174 offset:34560
	ds_read_b128 v[98:101], v174 offset:34592
	ds_read_b128 v[110:113], v174 offset:34624
	ds_read_b128 v[106:109], v174 offset:34656
	ds_read_b128 v[114:117], v174 offset:34688
	ds_read_b128 v[122:125], v174 offset:34720
	ds_read_b128 v[118:121], v174 offset:34752
	ds_read_b128 v[126:129], v174 offset:34784
	v_mov_b32_dpp v66, v66 quad_perm:[1,0,3,2] row_mask:0xf bank_mask:0xf bound_ctrl:1
	v_mov_b32_e32 v131, v130
	v_fmac_f32_e32 v66, v175, v71
	s_nop 0
	v_permlane32_swap_b32_e32 v130, v131
	v_add_f32_dpp v66, v66, v66 quad_perm:[2,3,0,1] row_mask:0xf bank_mask:0xf bound_ctrl:1
	v_add_f32_e32 v130, v130, v131
	v_fmamk_f32 v65, v130, 0xbc800000, v65
	v_add_f32_dpp v66, v66, v66 row_half_mirror row_mask:0xf bank_mask:0xf bound_ctrl:1
	v_fmamk_f32 v64, v130, 0xbc800000, v64
	v_fmamk_f32 v63, v130, 0xbc800000, v63
	v_fmamk_f32 v62, v130, 0xbc800000, v62
	v_fmamk_f32 v61, v130, 0xbc800000, v61
	v_fmamk_f32 v60, v130, 0xbc800000, v60
	v_fmamk_f32 v59, v130, 0xbc800000, v59
	v_fmamk_f32 v58, v130, 0xbc800000, v58
	v_fmamk_f32 v57, v130, 0xbc800000, v57
	v_fmamk_f32 v56, v130, 0xbc800000, v56
	v_fmamk_f32 v55, v130, 0xbc800000, v55
	v_fmamk_f32 v54, v130, 0xbc800000, v54
	v_fmamk_f32 v53, v130, 0xbc800000, v53
	v_fmamk_f32 v52, v130, 0xbc800000, v52
	v_fmamk_f32 v51, v130, 0xbc800000, v51
	v_fmac_f32_e32 v50, 0xbc800000, v130
	v_add_f32_dpp v66, v66, v66 row_ror:8 row_mask:0xf bank_mask:0xf bound_ctrl:1
	v_fmamk_f32 v17, v130, 0xbc800000, v17
	v_fmamk_f32 v16, v130, 0xbc800000, v16
	v_fmamk_f32 v15, v130, 0xbc800000, v15
	v_fmamk_f32 v14, v130, 0xbc800000, v14
	v_fmamk_f32 v13, v130, 0xbc800000, v13
	v_fmamk_f32 v12, v130, 0xbc800000, v12
	v_fmamk_f32 v11, v130, 0xbc800000, v11
	v_fmamk_f32 v10, v130, 0xbc800000, v10
	v_fmamk_f32 v9, v130, 0xbc800000, v9
	v_fmamk_f32 v8, v130, 0xbc800000, v8
	v_fmamk_f32 v7, v130, 0xbc800000, v7
	v_fmamk_f32 v6, v130, 0xbc800000, v6
	v_fmamk_f32 v5, v130, 0xbc800000, v5
	v_fmamk_f32 v4, v130, 0xbc800000, v4
	v_fmamk_f32 v3, v130, 0xbc800000, v3
	v_fmac_f32_e32 v2, 0xbc800000, v130
	v_pk_mul_f32 v[130:131], v[54:55], v[54:55]
	v_pk_mul_f32 v[132:133], v[62:63], v[62:63]
	v_pk_mul_f32 v[138:139], v[50:51], v[50:51]
	v_pk_mul_f32 v[140:141], v[58:59], v[58:59]
	v_pk_mul_f32 v[142:143], v[56:57], v[56:57]
	v_pk_mul_f32 v[144:145], v[64:65], v[64:65]
	v_pk_mul_f32 v[146:147], v[52:53], v[52:53]
	v_pk_mul_f32 v[148:149], v[60:61], v[60:61]
	v_mov_b32_e32 v67, v66
	v_pk_fma_f32 v[148:149], v[12:13], v[12:13], v[148:149]
	v_pk_fma_f32 v[146:147], v[4:5], v[4:5], v[146:147]
	v_pk_fma_f32 v[144:145], v[16:17], v[16:17], v[144:145]
	v_pk_fma_f32 v[142:143], v[8:9], v[8:9], v[142:143]
	v_pk_fma_f32 v[140:141], v[10:11], v[10:11], v[140:141]
	v_pk_fma_f32 v[138:139], v[2:3], v[2:3], v[138:139]
	v_pk_fma_f32 v[132:133], v[14:15], v[14:15], v[132:133]
	v_pk_fma_f32 v[130:131], v[6:7], v[6:7], v[130:131]
	v_permlane16_swap_b32_e32 v66, v67
	v_pk_add_f32 v[130:131], v[130:131], v[132:133]
	v_pk_add_f32 v[132:133], v[138:139], v[140:141]
	v_pk_add_f32 v[138:139], v[142:143], v[144:145]
	v_pk_add_f32 v[140:141], v[146:147], v[148:149]
	v_mfma_f32_32x32x16_bf16 v[18:33], v[74:77], v[78:81], v[18:33]
	v_add_f32_e32 v136, v66, v67
	ds_read_b128 v[70:73], v134 offset:512
	ds_read_b128 v[66:69], v134 offset:544
	ds_read_b128 v[78:81], v134 offset:576
	ds_read_b128 v[74:77], v134 offset:608
	ds_read_b128 v[82:85], v134 offset:640
	ds_read_b128 v[90:93], v134 offset:672
	ds_read_b128 v[86:89], v134 offset:704
	ds_read_b128 v[94:97], v134 offset:736
	v_pk_add_f32 v[138:139], v[140:141], v[138:139]
	v_pk_add_f32 v[130:131], v[132:133], v[130:131]
	s_waitcnt lgkmcnt(8)
	v_pk_mul_f32 v[140:141], v[126:127], v[62:63]
	v_pk_mov_b32 v[132:133], v[130:131], v[138:139] op_sel:[1,0]
	v_mov_b32_e32 v131, v139
	v_pk_mul_f32 v[138:139], v[122:123], v[54:55]
	v_pk_mul_f32 v[142:143], v[114:115], v[50:51]
	v_pk_mul_f32 v[144:145], v[118:119], v[58:59]
	v_pk_mul_f32 v[146:147], v[124:125], v[56:57]
	v_pk_mul_f32 v[148:149], v[128:129], v[64:65]
	v_pk_mul_f32 v[154:155], v[116:117], v[52:53]
	v_pk_mul_f32 v[156:157], v[120:121], v[60:61]
	v_pk_fma_f32 v[154:155], v[104:105], v[4:5], v[154:155]
	v_pk_fma_f32 v[156:157], v[112:113], v[12:13], v[156:157]
	v_pk_fma_f32 v[148:149], v[108:109], v[16:17], v[148:149]
	v_pk_fma_f32 v[146:147], v[100:101], v[8:9], v[146:147]
	v_pk_fma_f32 v[144:145], v[110:111], v[10:11], v[144:145]
	v_pk_fma_f32 v[142:143], v[102:103], v[2:3], v[142:143]
	v_pk_fma_f32 v[140:141], v[106:107], v[14:15], v[140:141]
	v_pk_fma_f32 v[138:139], v[98:99], v[6:7], v[138:139]
	v_pk_add_f32 v[130:131], v[132:133], v[130:131]
	v_pk_add_f32 v[138:139], v[138:139], v[140:141]
	v_pk_add_f32 v[140:141], v[142:143], v[144:145]
	v_pk_add_f32 v[142:143], v[146:147], v[148:149]
	v_pk_add_f32 v[144:145], v[154:155], v[156:157]
	v_pk_add_f32 v[132:133], v[130:131], v[130:131] op_sel:[0,1] op_sel_hi:[1,0]
	v_pk_add_f32 v[142:143], v[144:145], v[142:143]
	v_pk_add_f32 v[138:139], v[140:141], v[138:139]
	v_add_f32_e32 v133, v142, v143
	v_add_f32_e32 v130, v138, v139
	s_waitcnt lgkmcnt(2)
	v_pk_mul_f32 v[138:139], v[90:91], v[54:55]
	s_waitcnt lgkmcnt(0)
	v_pk_mul_f32 v[140:141], v[94:95], v[62:63]
	v_pk_mul_f32 v[142:143], v[82:83], v[50:51]
	v_pk_mul_f32 v[144:145], v[86:87], v[58:59]
	v_pk_mul_f32 v[146:147], v[92:93], v[56:57]
	v_pk_mul_f32 v[148:149], v[96:97], v[64:65]
	v_pk_mul_f32 v[154:155], v[84:85], v[52:53]
	v_pk_mul_f32 v[156:157], v[88:89], v[60:61]
	v_add_f32_e32 v130, v130, v133
	v_pk_fma_f32 v[156:157], v[80:81], v[12:13], v[156:157]
	v_pk_fma_f32 v[154:155], v[72:73], v[4:5], v[154:155]
	v_pk_fma_f32 v[148:149], v[76:77], v[16:17], v[148:149]
	v_pk_fma_f32 v[146:147], v[68:69], v[8:9], v[146:147]
	v_pk_fma_f32 v[144:145], v[78:79], v[10:11], v[144:145]
	v_pk_fma_f32 v[142:143], v[70:71], v[2:3], v[142:143]
	v_pk_fma_f32 v[140:141], v[74:75], v[14:15], v[140:141]
	v_pk_fma_f32 v[138:139], v[66:67], v[6:7], v[138:139]
	v_mov_b32_e32 v133, v130
	v_pk_add_f32 v[138:139], v[138:139], v[140:141]
	v_pk_add_f32 v[140:141], v[142:143], v[144:145]
	v_pk_add_f32 v[142:143], v[146:147], v[148:149]
	v_pk_add_f32 v[144:145], v[154:155], v[156:157]
	v_permlane32_swap_b32_e32 v130, v133
	v_pk_add_f32 v[142:143], v[144:145], v[142:143]
	v_add_f32_e32 v160, v130, v133
	v_pk_add_f32 v[138:139], v[140:141], v[138:139]
	v_add_f32_e32 v133, v142, v143
	v_pk_add_f32 v[140:141], v[26:27], v[42:43]
	v_pk_add_f32 v[142:143], v[28:29], v[44:45]
	v_pk_add_f32 v[144:145], v[20:21], v[36:37]
	v_pk_add_f32 v[146:147], v[32:33], v[48:49]
	v_pk_add_f32 v[148:149], v[24:25], v[40:41]
	v_pk_add_f32 v[154:155], v[30:31], v[46:47]
	v_pk_add_f32 v[156:157], v[22:23], v[38:39]
	v_pk_add_f32 v[158:159], v[18:19], v[34:35]
	v_pk_add_f32 v[154:155], v[156:157], v[154:155]
	v_pk_add_f32 v[146:147], v[148:149], v[146:147]
	v_pk_add_f32 v[142:143], v[144:145], v[142:143]
	v_pk_add_f32 v[140:141], v[158:159], v[140:141]
	v_pk_add_f32 v[142:143], v[142:143], v[146:147]
	v_pk_add_f32 v[140:141], v[140:141], v[154:155]
	v_add_f32_e32 v130, v138, v139
	v_pk_mov_b32 v[144:145], v[140:141], v[142:143] op_sel:[1,0]
	v_mov_b32_e32 v141, v143
	v_pk_add_f32 v[140:141], v[144:145], v[140:141]
	v_add_f32_e32 v133, v130, v133
	v_pk_add_f32 v[140:141], v[140:141], v[140:141] op_sel:[0,1] op_sel_hi:[1,0]
	v_mov_b32_e32 v131, v132
	v_mov_b32_e32 v130, v140
	s_nop 1
	v_permlane32_swap_b32_e32 v140, v130
	v_add_f32_e32 v130, v140, v130
	v_fmamk_f32 v49, v130, 0xbc800000, v49
	v_fmamk_f32 v48, v130, 0xbc800000, v48
	v_fmamk_f32 v47, v130, 0xbc800000, v47
	v_fmamk_f32 v46, v130, 0xbc800000, v46
	v_fmamk_f32 v45, v130, 0xbc800000, v45
	v_fmamk_f32 v44, v130, 0xbc800000, v44
	v_fmamk_f32 v43, v130, 0xbc800000, v43
	v_fmamk_f32 v42, v130, 0xbc800000, v42
	v_fmamk_f32 v41, v130, 0xbc800000, v41
	v_fmamk_f32 v40, v130, 0xbc800000, v40
	v_fmamk_f32 v39, v130, 0xbc800000, v39
	v_fmamk_f32 v38, v130, 0xbc800000, v38
	v_fmamk_f32 v37, v130, 0xbc800000, v37
	v_fmamk_f32 v36, v130, 0xbc800000, v36
	v_fmamk_f32 v35, v130, 0xbc800000, v35
	v_fmac_f32_e32 v34, 0xbc800000, v130
	v_fmamk_f32 v33, v130, 0xbc800000, v33
	v_fmamk_f32 v32, v130, 0xbc800000, v32
	v_fmamk_f32 v31, v130, 0xbc800000, v31
	v_fmamk_f32 v30, v130, 0xbc800000, v30
	v_fmamk_f32 v29, v130, 0xbc800000, v29
	v_fmamk_f32 v28, v130, 0xbc800000, v28
	v_fmamk_f32 v27, v130, 0xbc800000, v27
	v_fmamk_f32 v26, v130, 0xbc800000, v26
	v_fmamk_f32 v25, v130, 0xbc800000, v25
	v_fmamk_f32 v24, v130, 0xbc800000, v24
	v_fmamk_f32 v23, v130, 0xbc800000, v23
	v_fmamk_f32 v22, v130, 0xbc800000, v22
	v_fmamk_f32 v21, v130, 0xbc800000, v21
	v_fmamk_f32 v20, v130, 0xbc800000, v20
	v_fmamk_f32 v19, v130, 0xbc800000, v19
	v_fmac_f32_e32 v18, 0xbc800000, v130
	v_pk_mul_f32 v[140:141], v[38:39], v[38:39]
	v_pk_mul_f32 v[142:143], v[46:47], v[46:47]
	v_pk_mul_f32 v[144:145], v[34:35], v[34:35]
	v_pk_mul_f32 v[146:147], v[42:43], v[42:43]
	v_pk_mul_f32 v[148:149], v[40:41], v[40:41]
	v_pk_mul_f32 v[154:155], v[48:49], v[48:49]
	v_pk_mul_f32 v[156:157], v[36:37], v[36:37]
	v_pk_mul_f32 v[158:159], v[44:45], v[44:45]
	v_pk_fma_f32 v[156:157], v[20:21], v[20:21], v[156:157]
	v_pk_fma_f32 v[158:159], v[28:29], v[28:29], v[158:159]
	v_pk_fma_f32 v[154:155], v[32:33], v[32:33], v[154:155]
	v_pk_fma_f32 v[148:149], v[24:25], v[24:25], v[148:149]
	v_pk_fma_f32 v[146:147], v[26:27], v[26:27], v[146:147]
	v_pk_fma_f32 v[144:145], v[18:19], v[18:19], v[144:145]
	v_pk_fma_f32 v[142:143], v[30:31], v[30:31], v[142:143]
	v_pk_fma_f32 v[140:141], v[22:23], v[22:23], v[140:141]
	v_permlane32_swap_b32_e32 v132, v131
	v_pk_add_f32 v[140:141], v[140:141], v[142:143]
	v_pk_add_f32 v[142:143], v[144:145], v[146:147]
	v_pk_add_f32 v[144:145], v[148:149], v[154:155]
	v_pk_add_f32 v[146:147], v[156:157], v[158:159]
	v_pk_add_f32 v[140:141], v[142:143], v[140:141]
	v_pk_add_f32 v[144:145], v[146:147], v[144:145]
	v_pk_mul_f32 v[122:123], v[122:123], v[38:39]
	v_pk_mov_b32 v[142:143], v[140:141], v[144:145] op_sel:[1,0]
	v_mov_b32_e32 v141, v145
	v_pk_add_f32 v[140:141], v[142:143], v[140:141]
	v_pk_mul_f32 v[126:127], v[126:127], v[46:47]
	v_pk_add_f32 v[140:141], v[140:141], v[140:141] op_sel:[0,1] op_sel_hi:[1,0]
	v_pk_mul_f32 v[114:115], v[114:115], v[34:35]
	v_mov_b32_e32 v130, v140
	s_nop 1
	v_permlane32_swap_b32_e32 v140, v130
	v_mov_b32_e32 v141, v132
	v_pk_add_f32 v[130:131], v[140:141], v[130:131]
	v_pk_mul_f32 v[118:119], v[118:119], v[42:43]
	v_pk_fma_f32 v[130:131], v[130:131], s[0:1], v[152:153] op_sel_hi:[1,0,0]
	v_pk_mul_f32 v[124:125], v[124:125], v[40:41]
	v_mul_f32_e32 v132, 0x4b800000, v131
	v_cmp_gt_f32_e32 vcc, s1, v131
	v_pk_mul_f32 v[128:129], v[128:129], v[48:49]
	v_pk_mul_f32 v[116:117], v[116:117], v[36:37]
	v_pk_mul_f32 v[120:121], v[120:121], v[44:45]
	v_cndmask_b32_e32 v131, v131, v132, vcc
	v_mul_f32_e32 v132, 0x4b800000, v130
	v_cmp_gt_f32_e64 s[0:1], s1, v130
	v_pk_fma_f32 v[112:113], v[112:113], v[28:29], v[120:121]
	v_pk_fma_f32 v[104:105], v[104:105], v[20:21], v[116:117]
	v_pk_fma_f32 v[108:109], v[108:109], v[32:33], v[128:129]
	v_pk_fma_f32 v[100:101], v[100:101], v[24:25], v[124:125]
	v_pk_fma_f32 v[110:111], v[110:111], v[26:27], v[118:119]
	v_pk_fma_f32 v[102:103], v[102:103], v[18:19], v[114:115]
	v_pk_fma_f32 v[106:107], v[106:107], v[30:31], v[126:127]
	v_pk_fma_f32 v[98:99], v[98:99], v[22:23], v[122:123]
	v_rsq_f32_e32 v131, v131
	v_cndmask_b32_e64 v130, v130, v132, s[0:1]
	v_pk_add_f32 v[98:99], v[98:99], v[106:107]
	v_pk_add_f32 v[102:103], v[102:103], v[110:111]
	v_pk_add_f32 v[100:101], v[100:101], v[108:109]
	v_pk_add_f32 v[104:105], v[104:105], v[112:113]
	v_rsq_f32_e32 v132, v130
	v_pk_add_f32 v[100:101], v[104:105], v[100:101]
	v_pk_add_f32 v[98:99], v[102:103], v[98:99]
	v_mul_f32_e32 v130, 0x45800000, v131
	v_add_f32_e32 v98, v98, v99
	v_add_f32_e32 v99, v100, v101
	v_add_f32_e32 v98, v98, v99
	v_mov_b32_e32 v99, v98
	v_pk_mul_f32 v[90:91], v[90:91], v[38:39]
	v_pk_mul_f32 v[94:95], v[94:95], v[46:47]
	v_pk_mul_f32 v[82:83], v[82:83], v[34:35]
	v_pk_mul_f32 v[86:87], v[86:87], v[42:43]
	v_cndmask_b32_e32 v130, v131, v130, vcc
	v_mul_f32_e32 v131, 0x45800000, v132
	v_permlane32_swap_b32_e32 v98, v99
	v_pk_fma_f32 v[78:79], v[78:79], v[26:27], v[86:87]
	v_pk_fma_f32 v[70:71], v[70:71], v[18:19], v[82:83]
	v_pk_fma_f32 v[74:75], v[74:75], v[30:31], v[94:95]
	v_pk_fma_f32 v[66:67], v[66:67], v[22:23], v[90:91]
	v_cndmask_b32_e64 v131, v132, v131, s[0:1]
	v_add_f32_e32 v98, v98, v99
	v_pk_add_f32 v[66:67], v[66:67], v[74:75]
	v_pk_add_f32 v[70:71], v[70:71], v[78:79]
	v_mul_f32_e32 v139, v160, v130
	v_mul_f32_e32 v98, v98, v131
	v_pk_add_f32 v[66:67], v[70:71], v[66:67]
	v_cmp_gt_u32_e32 vcc, 32, v1
	v_add_f32_e32 v66, v66, v67
	v_pk_mul_f32 v[92:93], v[92:93], v[40:41]
	v_cndmask_b32_e32 v67, v98, v139, vcc
	v_add_f32_e32 v67, s12, v67
	v_pk_mul_f32 v[96:97], v[96:97], v[48:49]
	v_pk_mul_f32 v[84:85], v[84:85], v[36:37]
	v_pk_mul_f32 v[88:89], v[88:89], v[44:45]
	v_mul_f32_e32 v67, 0xbfb8aa3b, v67
	v_pk_fma_f32 v[80:81], v[80:81], v[28:29], v[88:89]
	v_pk_fma_f32 v[72:73], v[72:73], v[20:21], v[84:85]
	v_pk_fma_f32 v[76:77], v[76:77], v[32:33], v[96:97]
	v_pk_fma_f32 v[68:69], v[68:69], v[24:25], v[92:93]
	v_exp_f32_e32 v70, v67
	v_pk_add_f32 v[68:69], v[68:69], v[76:77]
	v_pk_add_f32 v[72:73], v[72:73], v[80:81]
	v_cmp_lt_i32_e64 s[0:1], 0, v151
	v_pk_add_f32 v[68:69], v[72:73], v[68:69]
	v_mov_b32_e32 v137, v136
	v_add_f32_e32 v67, v68, v69
	v_add_f32_e32 v67, v66, v67
	v_add_f32_e32 v66, 1.0, v70
	v_rcp_f32_e32 v66, v66
	v_mov_b32_e32 v69, 0xff800000
	v_mov_b32_e32 v138, v133
	v_mov_b32_e32 v68, v67
	v_cndmask_b32_e64 v70, v69, v66, s[0:1]
	v_mbcnt_lo_u32_b32 v66, -1, 0
	v_mbcnt_hi_u32_b32 v66, -1, v66
	v_permlane32_swap_b32_e32 v136, v137
	v_permlane32_swap_b32_e32 v133, v138
	v_permlane32_swap_b32_e32 v67, v68
	v_and_b32_e32 v86, 64, v66
	v_mov_b32_e32 v71, 8
	v_mov_b32_e32 v66, 0
.LBB1_9:
	v_max_f32_dpp v72, v70, v70 quad_perm:[1,0,3,2] row_mask:0xf bank_mask:0xf bound_ctrl:1
	s_nop 1
	v_max_f32_dpp v72, v72, v72 quad_perm:[2,3,0,1] row_mask:0xf bank_mask:0xf bound_ctrl:1
	s_nop 1
	v_max_f32_dpp v72, v72, v72 row_half_mirror row_mask:0xf bank_mask:0xf bound_ctrl:1
	s_nop 1
	v_max_f32_dpp v72, v72, v72 row_ror:8 row_mask:0xf bank_mask:0xf bound_ctrl:1
	v_mov_b32_e32 v73, v72
	s_nop 1
	v_permlane16_swap_b32_e32 v72, v73
	v_max_f32_e32 v72, v72, v73
	v_mov_b32_e32 v73, v72
	s_nop 1
	v_permlane32_swap_b32_e32 v72, v73
	v_max_f32_e32 v72, v72, v73
	v_cmp_eq_f32_e64 s[0:1], v70, v72
	s_ff1_i32_b64 s4, s[0:1]
	s_cmp_lg_u64 s[0:1], 0
	s_cselect_b32 s0, s4, -1
	v_and_or_b32 v72, s0, 63, v86
	v_lshlrev_b32_e32 v72, 2, v72
	ds_bpermute_b32 v72, v72, v151
	s_add_i32 s1, s13, 1
	s_cmp_gt_u32 s13, 6
	s_cselect_b64 s[14:15], -1, 0
	s_mov_b32 s13, s1
	s_waitcnt lgkmcnt(0)
	v_min_i32_e32 v72, v72, v71
	v_sub_u32_e32 v71, v71, v72
	v_cmp_gt_i32_e64 s[4:5], 1, v71
	s_or_b64 s[4:5], s[14:15], s[4:5]
	v_cmp_eq_u32_e64 s[0:1], s0, v1
	s_and_b64 s[4:5], exec, s[4:5]
	s_or_b64 s[6:7], s[4:5], s[6:7]
	v_cndmask_b32_e64 v66, v66, v72, s[0:1]
	v_cndmask_b32_e64 v70, v70, v69, s[0:1]
	s_andn2_b64 exec, exec, s[6:7]
	s_cbranch_execnz .LBB1_9
	s_or_b64 exec, exec, s[6:7]
	v_add_f32_e32 v69, v133, v138
	v_add_f32_e32 v67, v67, v68
	v_mul_f32_e32 v69, v69, v130
	v_mul_f32_e32 v67, v67, v131
	v_add_f32_e32 v68, v136, v137
	v_cndmask_b32_e32 v67, v67, v69, vcc
	v_add_f32_e32 v67, v68, v67
	v_mul_f32_e32 v68, 0x3e000000, v67
	v_mov_b32_e32 v69, 0xff800000
	v_cmp_lt_i32_e64 s[0:1], 0, v66
	s_mov_b32 s4, 0x3e000000
	v_cvt_f32_u32_e32 v66, v66
	v_cndmask_b32_e64 v68, v69, v68, s[0:1]
	v_cvt_pk_bf16_f32 v9, v8, v9
	v_cvt_pk_bf16_f32 v8, v6, v7
	v_max_f32_dpp v68, v68, v68 quad_perm:[1,0,3,2] row_mask:0xf bank_mask:0xf bound_ctrl:1
	v_cvt_pk_bf16_f32 v6, v2, v3
	s_nop 0
	v_max_f32_dpp v68, v68, v68 quad_perm:[2,3,0,1] row_mask:0xf bank_mask:0xf bound_ctrl:1
	v_cvt_pk_bf16_f32 v7, v4, v5
	s_nop 0
	v_max_f32_dpp v68, v68, v68 row_half_mirror row_mask:0xf bank_mask:0xf bound_ctrl:1
	v_cvt_pk_bf16_f32 v91, v16, v17
	v_cvt_pk_bf16_f32 v90, v14, v15
	v_max_f32_dpp v68, v68, v68 row_ror:8 row_mask:0xf bank_mask:0xf bound_ctrl:1
	v_mov_b32_e32 v69, v68
	s_nop 1
	v_permlane16_swap_b32_e32 v68, v69
	v_max_f32_e32 v68, v68, v69
	v_mov_b32_e32 v69, v68
	s_nop 1
	v_permlane32_swap_b32_e32 v68, v69
	v_max_f32_e32 v68, v68, v69
	v_fma_f32 v67, v67, s4, -v68
	v_mul_f32_e32 v67, 0x3fb8aa3b, v67
	v_exp_f32_e32 v67, v67
	v_cvt_pk_bf16_f32 v89, v12, v13
	v_cvt_pk_bf16_f32 v88, v10, v11
	v_mul_f32_e32 v66, v67, v66
	v_cndmask_b32_e64 v66, 0, v66, s[0:1]
	v_cvt_pk_bf16_f32 v57, v56, v57
	v_cvt_pk_bf16_f32 v56, v54, v55
	v_add_f32_dpp v67, v66, v66 quad_perm:[1,0,3,2] row_mask:0xf bank_mask:0xf bound_ctrl:1
	v_cvt_pk_bf16_f32 v54, v50, v51
	v_cvt_pk_bf16_f32 v50, v58, v59
	v_add_f32_dpp v67, v67, v67 quad_perm:[2,3,0,1] row_mask:0xf bank_mask:0xf bound_ctrl:1
	v_cvt_pk_bf16_f32 v55, v52, v53
	s_nop 0
	v_add_f32_dpp v67, v67, v67 row_half_mirror row_mask:0xf bank_mask:0xf bound_ctrl:1
	v_cvt_pk_bf16_f32 v53, v64, v65
	v_cvt_pk_bf16_f32 v52, v62, v63
	v_add_f32_dpp v67, v67, v67 row_ror:8 row_mask:0xf bank_mask:0xf bound_ctrl:1
	v_mov_b32_e32 v68, v67
	s_nop 1
	v_permlane16_swap_b32_e32 v67, v68
	v_add_f32_e32 v67, v67, v68
	v_mov_b32_e32 v68, v67
	s_nop 1
	v_permlane32_swap_b32_e32 v67, v68
	v_add_f32_e32 v67, v67, v68
	v_rcp_f32_e32 v67, v67
	v_cvt_pk_bf16_f32 v51, v60, v61
	v_cvt_pk_bf16_f32 v25, v24, v25
	v_cvt_pk_bf16_f32 v24, v22, v23
	v_mul_f32_e32 v66, v66, v67
	v_cndmask_b32_e32 v67, v131, v130, vcc
	v_mul_f32_e32 v66, v67, v66
	ds_write_b32 v173, v66 offset:768
	s_waitcnt lgkmcnt(0)
	ds_read_b128 v[82:85], v212 offset:27648
	ds_read_b128 v[92:95], v212 offset:28672
	ds_read_b128 v[96:99], v212 offset:31744
	ds_read_b128 v[100:103], v212 offset:32768
	s_waitcnt lgkmcnt(3)
	v_mfma_f32_32x32x16_bf16 v[66:81], v[6:9], v[82:85], 0
	ds_read_b128 v[104:107], v212 offset:29696
	ds_read_b32 v87, v135 offset:34816
	v_cvt_pk_bf16_f32 v23, v20, v21
	v_cvt_pk_bf16_f32 v22, v18, v19
	v_cvt_pk_bf16_f32 v119, v32, v33
	v_cvt_pk_bf16_f32 v118, v30, v31
	v_cvt_pk_bf16_f32 v117, v28, v29
	s_waitcnt lgkmcnt(3)
	v_mfma_f32_32x32x16_bf16 v[2:17], v[6:9], v[96:99], 0
	v_cvt_pk_bf16_f32 v116, v26, v27
	v_cvt_pk_bf16_f32 v41, v40, v41
	v_cvt_pk_bf16_f32 v40, v38, v39
	v_cvt_pk_bf16_f32 v39, v36, v37
	v_cvt_pk_bf16_f32 v38, v34, v35
	v_cvt_pk_bf16_f32 v37, v48, v49
	v_cvt_pk_bf16_f32 v36, v46, v47
	v_mfma_f32_32x32x16_bf16 v[66:81], v[88:91], v[92:95], v[66:81]
	v_cvt_pk_bf16_f32 v35, v44, v45
	v_cvt_pk_bf16_f32 v34, v42, v43
	s_waitcnt lgkmcnt(2)
	v_mfma_f32_32x32x16_bf16 v[2:17], v[88:91], v[100:103], v[2:17]
	ds_read_b128 v[88:91], v212 offset:30720
	ds_read_b128 v[108:111], v212 offset:33792
	s_waitcnt lgkmcnt(3)
	v_mfma_f32_32x32x16_bf16 v[66:81], v[54:57], v[104:107], v[66:81]
	s_waitcnt lgkmcnt(0)
	v_mfma_f32_32x32x16_bf16 v[2:17], v[54:57], v[108:111], v[2:17]
	ds_read_b128 v[112:115], v212 offset:34816
	v_mfma_f32_32x32x16_bf16 v[66:81], v[50:53], v[88:91], v[66:81]
	s_waitcnt lgkmcnt(0)
	v_mfma_f32_32x32x16_bf16 v[2:17], v[50:53], v[112:115], v[2:17]
	v_mfma_f32_32x32x16_bf16 v[50:65], v[22:25], v[82:85], 0
	v_mfma_f32_32x32x16_bf16 v[18:33], v[22:25], v[96:99], 0
	v_mfma_f32_32x32x16_bf16 v[50:65], v[116:119], v[92:95], v[50:65]
	v_mfma_f32_32x32x16_bf16 v[18:33], v[116:119], v[100:103], v[18:33]
	v_mfma_f32_32x32x16_bf16 v[50:65], v[38:41], v[104:107], v[50:65]
	v_mfma_f32_32x32x16_bf16 v[18:33], v[38:41], v[108:111], v[18:33]
	ds_read_b128 v[38:41], v134 offset:896
	ds_read_b128 v[42:45], v134 offset:928
	v_mfma_f32_32x32x16_bf16 v[50:65], v[34:37], v[88:91], v[50:65]
	v_mfma_f32_32x32x16_bf16 v[18:33], v[34:37], v[112:115], v[18:33]
	ds_read_b128 v[34:37], v134 offset:960
	ds_read_b128 v[46:49], v134 offset:992
	ds_read_b128 v[82:85], v134 offset:768
	ds_read_b128 v[88:91], v134 offset:800
	ds_read_b128 v[92:95], v134 offset:832
	ds_read_b128 v[96:99], v134 offset:864
	s_waitcnt lgkmcnt(6)
	s_nop 3
	v_pk_mul_f32 v[54:55], v[42:43], v[54:55]
	s_waitcnt lgkmcnt(4)
	v_pk_mul_f32 v[62:63], v[46:47], v[62:63]
	v_pk_mul_f32 v[56:57], v[44:45], v[56:57]
	v_pk_mul_f32 v[64:65], v[48:49], v[64:65]
	v_pk_mul_f32 v[52:53], v[40:41], v[52:53]
	v_pk_mul_f32 v[60:61], v[36:37], v[60:61]
	v_pk_mul_f32 v[58:59], v[34:35], v[58:59]
	v_pk_mul_f32 v[50:51], v[38:39], v[50:51]
	v_pk_mul_f32 v[22:23], v[42:43], v[22:23]
	v_pk_mul_f32 v[30:31], v[46:47], v[30:31]
	v_pk_mul_f32 v[24:25], v[44:45], v[24:25]
	v_pk_mul_f32 v[32:33], v[48:49], v[32:33]
	v_pk_mul_f32 v[20:21], v[40:41], v[20:21]
	v_pk_mul_f32 v[28:29], v[36:37], v[28:29]
	v_pk_mul_f32 v[26:27], v[34:35], v[26:27]
	v_pk_mul_f32 v[18:19], v[38:39], v[18:19]
	s_waitcnt lgkmcnt(1)
	v_pk_fma_f32 v[58:59], v[92:93], v[74:75], v[58:59]
	v_pk_fma_f32 v[60:61], v[94:95], v[76:77], v[60:61]
	v_pk_fma_f32 v[52:53], v[84:85], v[68:69], v[52:53]
	s_waitcnt lgkmcnt(0)
	v_pk_fma_f32 v[64:65], v[98:99], v[80:81], v[64:65]
	v_pk_fma_f32 v[56:57], v[90:91], v[72:73], v[56:57]
	v_pk_fma_f32 v[62:63], v[96:97], v[78:79], v[62:63]
	v_pk_fma_f32 v[54:55], v[88:89], v[70:71], v[54:55]
	v_pk_fma_f32 v[50:51], v[82:83], v[66:67], v[50:51]
	v_pk_fma_f32 v[10:11], v[92:93], v[10:11], v[26:27]
	v_pk_fma_f32 v[12:13], v[94:95], v[12:13], v[28:29]
	v_pk_fma_f32 v[4:5], v[84:85], v[4:5], v[20:21]
	v_pk_fma_f32 v[16:17], v[98:99], v[16:17], v[32:33]
	v_pk_fma_f32 v[8:9], v[90:91], v[8:9], v[24:25]
	v_pk_fma_f32 v[14:15], v[96:97], v[14:15], v[30:31]
	v_pk_fma_f32 v[6:7], v[88:89], v[6:7], v[22:23]
	v_pk_fma_f32 v[2:3], v[82:83], v[2:3], v[18:19]
	v_pk_add_f32 v[54:55], v[54:55], v[62:63]
	v_pk_add_f32 v[56:57], v[56:57], v[64:65]
	v_pk_add_f32 v[52:53], v[52:53], v[60:61]
	v_pk_add_f32 v[50:51], v[50:51], v[58:59]
	v_pk_add_f32 v[6:7], v[6:7], v[14:15]
	v_pk_add_f32 v[8:9], v[8:9], v[16:17]
	v_pk_add_f32 v[4:5], v[4:5], v[12:13]
	v_pk_add_f32 v[2:3], v[2:3], v[10:11]
	v_pk_add_f32 v[52:53], v[52:53], v[56:57]
	v_pk_add_f32 v[50:51], v[50:51], v[54:55]
	v_pk_add_f32 v[4:5], v[4:5], v[8:9]
	v_pk_add_f32 v[2:3], v[2:3], v[6:7]
	v_add_f32_e32 v50, v50, v51
	v_add_f32_e32 v51, v52, v53
	v_add_f32_e32 v2, v2, v3
	v_add_f32_e32 v3, v4, v5
	v_add_f32_e32 v50, v50, v51
	v_add_f32_e32 v2, v2, v3
	v_mov_b32_e32 v3, v50
	v_mov_b32_e32 v4, v2
	s_nop 0
	v_permlane32_swap_b32_e32 v50, v3
	v_permlane32_swap_b32_e32 v2, v4
	v_add_f32_e32 v3, v50, v3
	v_add_f32_e32 v2, v2, v4
	v_cndmask_b32_e32 v2, v2, v3, vcc
	v_add_f32_e32 v3, v87, v2
	v_cmp_eq_u32_e32 vcc, 0, v1
	s_nop 0
	v_max_f32_dpp v2, v3, v3 quad_perm:[1,0,3,2] row_mask:0xf bank_mask:0xf bound_ctrl:1
	s_nop 1
	v_max_f32_dpp v2, v2, v2 quad_perm:[2,3,0,1] row_mask:0xf bank_mask:0xf bound_ctrl:1
	s_nop 1
	v_max_f32_dpp v2, v2, v2 row_half_mirror row_mask:0xf bank_mask:0xf bound_ctrl:1
	s_nop 1
	v_max_f32_dpp v2, v2, v2 row_ror:8 row_mask:0xf bank_mask:0xf bound_ctrl:1
	v_mov_b32_e32 v4, v2
	s_nop 1
	v_permlane16_swap_b32_e32 v2, v4
	v_max_f32_e32 v2, v2, v4
	v_mov_b32_e32 v4, v2
	s_nop 1
	v_permlane32_swap_b32_e32 v2, v4
	v_max_f32_e32 v2, v2, v4
	v_sub_f32_e32 v4, v3, v2
	v_mul_f32_e32 v4, 0x3fb8aa3b, v4
	v_exp_f32_e32 v4, v4
	s_nop 1
	v_add_f32_dpp v4, v4, v4 quad_perm:[1,0,3,2] row_mask:0xf bank_mask:0xf bound_ctrl:1
	s_nop 1
	v_add_f32_dpp v4, v4, v4 quad_perm:[2,3,0,1] row_mask:0xf bank_mask:0xf bound_ctrl:1
	s_nop 1
	v_add_f32_dpp v4, v4, v4 row_half_mirror row_mask:0xf bank_mask:0xf bound_ctrl:1
	s_nop 1
	v_add_f32_dpp v4, v4, v4 row_ror:8 row_mask:0xf bank_mask:0xf bound_ctrl:1
	v_mov_b32_e32 v5, v4
	s_nop 1
	v_permlane16_swap_b32_e32 v4, v5
	v_add_f32_e32 v4, v4, v5
	v_and_or_b32 v5, s3, 63, v86
	v_lshlrev_b32_e32 v5, 2, v5
	ds_bpermute_b32 v3, v5, v3
	v_mov_b32_e32 v5, v4
	s_nop 1
	v_permlane32_swap_b32_e32 v4, v5
	s_and_saveexec_b64 s[4:5], vcc
	s_cbranch_execz .LBB1_12
	v_add_f32_e32 v1, v4, v5
	s_mov_b32 s0, 0x800000
	v_cmp_gt_f32_e32 vcc, s0, v1
	s_mov_b32 s0, 0x3f317217
	s_nop 0
	v_cndmask_b32_e64 v4, 0, 32, vcc
	v_ldexp_f32 v1, v1, v4
	v_log_f32_e32 v1, v1
	s_nop 0
	v_mul_f32_e32 v4, 0x3f317217, v1
	v_fma_f32 v4, v1, s0, -v4
	v_fmamk_f32 v4, v1, 0x3377d1cf, v4
	s_mov_b32 s0, 0x7f800000
	v_fmac_f32_e32 v4, 0x3f317217, v1
	v_cmp_lt_f32_e64 s[0:1], |v1|, s0
	s_nop 1
	v_cndmask_b32_e64 v1, v1, v4, s[0:1]
	v_mov_b32_e32 v4, 0x41b17218
	v_cndmask_b32_e32 v4, 0, v4, vcc
	v_sub_f32_e32 v1, v1, v4
	v_add_f32_e32 v1, v2, v1
	s_waitcnt lgkmcnt(0)
	v_sub_f32_e32 v1, v1, v3
	ds_write_b32 v172, v1

	.amdhsa_kernel _Z9fast_mainILb0EEvPKiS1_S1_PKfPKcS3_PfS6_PiPyS6_
		.amdhsa_group_segment_fixed_size 150528
		.amdhsa_private_segment_fixed_size 0
		.amdhsa_kernarg_size 88
		.amdhsa_user_sgpr_count 2
		.amdhsa_user_sgpr_dispatch_ptr 0
		.amdhsa_user_sgpr_queue_ptr 0
		.amdhsa_user_sgpr_kernarg_segment_ptr 1
		.amdhsa_user_sgpr_dispatch_id 0
		.amdhsa_user_sgpr_kernarg_preload_length 0
		.amdhsa_user_sgpr_kernarg_preload_offset 0
		.amdhsa_user_sgpr_private_segment_size 0
		.amdhsa_uses_dynamic_stack 0
		.amdhsa_enable_private_segment 0
		.amdhsa_system_sgpr_workgroup_id_x 1
		.amdhsa_system_sgpr_workgroup_id_y 0
		.amdhsa_system_sgpr_workgroup_id_z 0
		.amdhsa_system_sgpr_workgroup_info 0
		.amdhsa_system_vgpr_workitem_id 0
		.amdhsa_next_free_vgpr 216
		.amdhsa_next_free_sgpr 96
		.amdhsa_accum_offset 216
		.amdhsa_reserve_vcc 1
		.amdhsa_float_round_mode_32 0
		.amdhsa_float_round_mode_16_64 0
		.amdhsa_float_denorm_mode_32 3
		.amdhsa_float_denorm_mode_16_64 3
		.amdhsa_dx10_clamp 1
		.amdhsa_ieee_mode 1
		.amdhsa_fp16_overflow 0
		.amdhsa_tg_split 0
		.amdhsa_exception_fp_ieee_invalid_op 0
		.amdhsa_exception_fp_denorm_src 0
		.amdhsa_exception_fp_ieee_div_zero 0
		.amdhsa_exception_fp_ieee_overflow 0
		.amdhsa_exception_fp_ieee_underflow 0
		.amdhsa_exception_fp_ieee_inexact 0
		.amdhsa_exception_int_div_zero 0
	.end_amdhsa_kernel

amdhsa.kernels:
  - .agpr_count:     16
    .args:
      - .actual_access:  read_only
        .address_space:  global
        .offset:         0
        .size:           8
        .value_kind:     global_buffer
      - .actual_access:  read_only
        .address_space:  global
        .offset:         8
        .size:           8
        .value_kind:     global_buffer
      - .actual_access:  read_only
        .address_space:  global
        .offset:         16
        .size:           8
        .value_kind:     global_buffer
      - .actual_access:  read_only
        .address_space:  global
        .offset:         24
        .size:           8
        .value_kind:     global_buffer
      - .actual_access:  read_only
        .address_space:  global
        .offset:         32
        .size:           8
        .value_kind:     global_buffer
      - .actual_access:  read_only
        .address_space:  global
        .offset:         40
        .size:           8
        .value_kind:     global_buffer
      - .actual_access:  read_only
        .address_space:  global
        .offset:         48
        .size:           8
        .value_kind:     global_buffer
      - .actual_access:  read_only
        .address_space:  global
        .offset:         56
        .size:           8
        .value_kind:     global_buffer
      - .actual_access:  read_only
        .address_space:  global
        .offset:         64
        .size:           8
        .value_kind:     global_buffer
      - .actual_access:  read_only
        .address_space:  global
        .offset:         72
        .size:           8
        .value_kind:     global_buffer
      - .actual_access:  read_only
        .address_space:  global
        .offset:         80
        .size:           8
        .value_kind:     global_buffer
      - .actual_access:  read_only
        .address_space:  global
        .offset:         88
        .size:           8
        .value_kind:     global_buffer
      - .actual_access:  read_only
        .address_space:  global
        .offset:         96
        .size:           8
        .value_kind:     global_buffer
      - .actual_access:  read_only
        .address_space:  global
        .offset:         104
        .size:           8
        .value_kind:     global_buffer
      - .actual_access:  read_only
        .address_space:  global
        .offset:         112
        .size:           8
        .value_kind:     global_buffer
      - .actual_access:  read_only
        .address_space:  global
        .offset:         120
        .size:           8
        .value_kind:     global_buffer
      - .actual_access:  read_only
        .address_space:  global
        .offset:         128
        .size:           8
        .value_kind:     global_buffer
      - .actual_access:  read_only
        .address_space:  global
        .offset:         136
        .size:           8
        .value_kind:     global_buffer
      - .actual_access:  read_only
        .address_space:  global
        .offset:         144
        .size:           8
        .value_kind:     global_buffer
      - .actual_access:  write_only
        .address_space:  global
        .offset:         152
        .size:           8
        .value_kind:     global_buffer
      - .actual_access:  write_only
        .address_space:  global
        .offset:         160
        .size:           8
        .value_kind:     global_buffer
      - .actual_access:  write_only
        .address_space:  global
        .offset:         168
        .size:           8
        .value_kind:     global_buffer
      - .actual_access:  read_only
        .address_space:  global
        .offset:         176
        .size:           8
        .value_kind:     global_buffer
    .group_segment_fixed_size: 0
    .kernarg_segment_align: 8
    .kernarg_segment_size: 184
    .language:       OpenCL C
    .language_version:
      - 2
      - 0
    .max_flat_workgroup_size: 64
    .name:           _Z11prep_tablesPKfS0_S0_S0_S0_S0_S0_S0_S0_S0_S0_S0_S0_S0_S0_S0_S0_S0_S0_PcPfPyS0_
    .private_segment_fixed_size: 0
    .sgpr_count:     80
    .sgpr_spill_count: 0
    .symbol:         _Z11prep_tablesPKfS0_S0_S0_S0_S0_S0_S0_S0_S0_S0_S0_S0_S0_S0_S0_S0_S0_S0_PcPfPyS0_.kd
    .uniform_work_group_size: 1
    .uses_dynamic_stack: false
    .vgpr_count:     100
    .vgpr_spill_count: 0
    .wavefront_size: 64
  - .agpr_count:     0
    .args:
      - .actual_access:  read_only
        .address_space:  global
        .offset:         0
        .size:           8
        .value_kind:     global_buffer
      - .actual_access:  read_only
        .address_space:  global
        .offset:         8
        .size:           8
        .value_kind:     global_buffer
      - .actual_access:  read_only
        .address_space:  global
        .offset:         16
        .size:           8
        .value_kind:     global_buffer
      - .actual_access:  read_only
        .address_space:  global
        .offset:         24
        .size:           8
        .value_kind:     global_buffer
      - .address_space:  global
        .offset:         32
        .size:           8
        .value_kind:     global_buffer
      - .actual_access:  read_only
        .address_space:  global
        .offset:         40
        .size:           8
        .value_kind:     global_buffer
      - .actual_access:  read_only
        .address_space:  global
        .offset:         48
        .size:           8
        .value_kind:     global_buffer
      - .actual_access:  read_only
        .address_space:  global
        .offset:         56
        .size:           8
        .value_kind:     global_buffer
      - .actual_access:  read_only
        .address_space:  global
        .offset:         64
        .size:           8
        .value_kind:     global_buffer
      - .address_space:  global
        .offset:         72
        .size:           8
        .value_kind:     global_buffer
      - .actual_access:  write_only
        .address_space:  global
        .offset:         80
        .size:           8
        .value_kind:     global_buffer
    .group_segment_fixed_size: 150528
    .kernarg_segment_align: 8
    .kernarg_segment_size: 88
    .language:       OpenCL C
    .language_version:
      - 2
      - 0
    .max_flat_workgroup_size: 512
    .name:           _Z9fast_mainILb0EEvPKiS1_S1_PKfPKcS3_PfS6_PiPyS6_
    .private_segment_fixed_size: 0
    .sgpr_count:     22
    .sgpr_spill_count: 0
    .symbol:         _Z9fast_mainILb0EEvPKiS1_S1_PKfPKcS3_PfS6_PiPyS6_.kd
    .uniform_work_group_size: 1
    .uses_dynamic_stack: false
    .vgpr_count:     216
    .vgpr_spill_count: 0
    .wavefront_size: 64
